# GEMM K-loops: duplicate s_waitcnt lgkmcnt(0) behind each segment barrier dropped (the wait in front of the barrier already covers it)
# baseline (speedup 1.0000x reference)
.LBB0_180:
	ds_read_b128 v[170:173], v163
	ds_read_b128 v[174:177], v163 offset:1024
	ds_read_b128 v[178:181], v163 offset:2048
	ds_read_b128 v[182:185], v163 offset:3072
	ds_read_b128 v[186:189], v164
	ds_read_b128 v[190:193], v164 offset:1024
	ds_read_b128 v[194:197], v164 offset:2048
	ds_read_b128 v[198:201], v164 offset:3072
	s_add_u32 s54, s50, s4
	s_addc_u32 s55, s51, s5
	s_cmpk_eq_i32 s4, 0x1000
	s_cselect_b64 vcc, -1, 0
	s_and_b64 s[52:53], vcc, exec
	s_cselect_b32 s72, 0, s4
	s_cselect_b32 s71, 0, s5
	s_cselect_b32 s52, s47, s54
	s_cselect_b32 s53, s7, s55
	s_add_u32 s54, s18, s72
	v_cndmask_b32_e32 v140, v128, v166, vcc
	v_cndmask_b32_e32 v129, v132, v168, vcc
	v_cndmask_b32_e32 v154, v130, v167, vcc
	v_cndmask_b32_e32 v131, v134, v169, vcc
	s_addc_u32 s55, s19, s71
	v_lshl_add_u64 v[234:235], v[152:153], 0, s[4:5]
	v_lshl_add_u64 v[234:235], v[234:235], 0, s[14:15]
	s_add_i32 m0, s1, 0xc000
	ds_read_b128 v[202:205], v165
	ds_read_b128 v[206:209], v165 offset:1024
	ds_read_b128 v[210:213], v165 offset:2048
	ds_read_b128 v[214:217], v165 offset:3072
	ds_read_b128 v[218:221], v165 offset:4096
	ds_read_b128 v[222:225], v165 offset:5120
	ds_read_b128 v[226:229], v165 offset:6144
	ds_read_b128 v[230:233], v165 offset:7168
	global_load_lds_dwordx4 v[234:235], off
	v_lshl_add_u64 v[234:235], v[150:151], 0, s[4:5]
	v_lshl_add_u64 v[234:235], v[234:235], 0, s[14:15]
	s_add_i32 m0, s1, 0xe000
	s_nop 0
	global_load_lds_dwordx4 v[234:235], off
	s_waitcnt vmcnt(8)
	s_waitcnt lgkmcnt(0)
	s_barrier
	s_setprio 1
	v_mfma_f32_16x16x32_bf16 v[60:63], v[170:173], v[202:205], v[60:63]
	v_mfma_f32_16x16x32_bf16 v[56:59], v[178:181], v[202:205], v[56:59]
	v_mfma_f32_16x16x32_bf16 v[52:55], v[170:173], v[210:213], v[52:55]
	v_mfma_f32_16x16x32_bf16 v[48:51], v[178:181], v[210:213], v[48:51]
	v_mfma_f32_16x16x32_bf16 v[44:47], v[170:173], v[218:221], v[44:47]
	v_mfma_f32_16x16x32_bf16 v[40:43], v[178:181], v[218:221], v[40:43]
	v_mfma_f32_16x16x32_bf16 v[36:39], v[170:173], v[226:229], v[36:39]
	v_mfma_f32_16x16x32_bf16 v[32:35], v[178:181], v[226:229], v[32:35]
	v_mfma_f32_16x16x32_bf16 v[60:63], v[174:177], v[206:209], v[60:63]
	v_mfma_f32_16x16x32_bf16 v[56:59], v[182:185], v[206:209], v[56:59]
	v_mfma_f32_16x16x32_bf16 v[52:55], v[174:177], v[214:217], v[52:55]
	v_mfma_f32_16x16x32_bf16 v[48:51], v[182:185], v[214:217], v[48:51]
	v_mfma_f32_16x16x32_bf16 v[44:47], v[174:177], v[222:225], v[44:47]
	v_mfma_f32_16x16x32_bf16 v[40:43], v[182:185], v[222:225], v[40:43]
	v_mfma_f32_16x16x32_bf16 v[36:39], v[174:177], v[230:233], v[36:39]
	v_mfma_f32_16x16x32_bf16 v[32:35], v[182:185], v[230:233], v[32:35]
	s_setprio 0
	s_setprio 1
	v_mfma_f32_16x16x32_bf16 v[124:127], v[186:189], v[202:205], v[124:127]
	v_mfma_f32_16x16x32_bf16 v[120:123], v[194:197], v[202:205], v[120:123]
	v_mfma_f32_16x16x32_bf16 v[116:119], v[186:189], v[210:213], v[116:119]
	v_mfma_f32_16x16x32_bf16 v[112:115], v[194:197], v[210:213], v[112:115]
	v_mfma_f32_16x16x32_bf16 v[108:111], v[186:189], v[218:221], v[108:111]
	v_mfma_f32_16x16x32_bf16 v[104:107], v[194:197], v[218:221], v[104:107]
	v_mfma_f32_16x16x32_bf16 v[100:103], v[186:189], v[226:229], v[100:103]
	v_mfma_f32_16x16x32_bf16 v[96:99], v[194:197], v[226:229], v[96:99]
	v_mfma_f32_16x16x32_bf16 v[124:127], v[190:193], v[206:209], v[124:127]
	v_mfma_f32_16x16x32_bf16 v[120:123], v[198:201], v[206:209], v[120:123]
	v_mfma_f32_16x16x32_bf16 v[116:119], v[190:193], v[214:217], v[116:119]
	v_mfma_f32_16x16x32_bf16 v[112:115], v[198:201], v[214:217], v[112:115]
	v_mfma_f32_16x16x32_bf16 v[108:111], v[190:193], v[222:225], v[108:111]
	v_mfma_f32_16x16x32_bf16 v[104:107], v[198:201], v[222:225], v[104:107]
	v_mfma_f32_16x16x32_bf16 v[100:103], v[190:193], v[230:233], v[100:103]
	v_mfma_f32_16x16x32_bf16 v[96:99], v[198:201], v[230:233], v[96:99]
	s_setprio 0
	s_barrier
	s_add_i32 s71, s66, s0
	v_lshl_add_u64 v[234:235], s[52:53], 0, v[136:137]
	s_mov_b32 m0, s71
	ds_read_b128 v[202:205], v165 offset:16384
	ds_read_b128 v[206:209], v165 offset:17408
	ds_read_b128 v[210:213], v165 offset:18432
	ds_read_b128 v[214:217], v165 offset:19456
	ds_read_b128 v[218:221], v165 offset:20480
	ds_read_b128 v[222:225], v165 offset:21504
	ds_read_b128 v[226:229], v165 offset:22528
	ds_read_b128 v[230:233], v165 offset:23552
	global_load_lds_dwordx4 v[234:235], off
	s_add_i32 m0, s71, 0x2000
	s_add_u32 s72, s52, 0x80000
	v_lshl_add_u64 v[236:237], s[52:53], 0, v[138:139]
	s_addc_u32 s73, s53, 0
	s_add_i32 s71, s67, s0
	global_load_lds_dwordx4 v[236:237], off
	v_lshl_add_u64 v[238:239], s[72:73], 0, v[136:137]
	s_mov_b32 m0, s71
	v_mov_b32_e32 v155, v141
	global_load_lds_dwordx4 v[238:239], off
	v_lshl_add_u64 v[238:239], s[72:73], 0, v[138:139]
	s_add_i32 m0, s71, 0x2000
	s_nop 0
	global_load_lds_dwordx4 v[238:239], off
	s_mov_b32 m0, s1
	v_lshl_add_u64 v[238:239], s[54:55], 0, v[140:141]
	global_load_lds_dwordx4 v140, s[54:55]
	s_mov_b32 m0, s8
	s_nop 0
	global_load_lds_dwordx4 v154, s[54:55]
	s_waitcnt vmcnt(8)
	s_waitcnt lgkmcnt(0)
	v_lshl_add_u64 v[154:155], s[54:55], 0, v[154:155]
	s_barrier
	s_setprio 1
	v_mfma_f32_16x16x32_bf16 v[28:31], v[170:173], v[202:205], v[28:31]
	v_mfma_f32_16x16x32_bf16 v[24:27], v[178:181], v[202:205], v[24:27]
	v_mfma_f32_16x16x32_bf16 v[20:23], v[170:173], v[210:213], v[20:23]
	v_mfma_f32_16x16x32_bf16 v[16:19], v[178:181], v[210:213], v[16:19]
	v_mfma_f32_16x16x32_bf16 v[12:15], v[170:173], v[218:221], v[12:15]
	v_mfma_f32_16x16x32_bf16 v[8:11], v[178:181], v[218:221], v[8:11]
	v_mfma_f32_16x16x32_bf16 v[4:7], v[170:173], v[226:229], v[4:7]
	v_mfma_f32_16x16x32_bf16 v[0:3], v[178:181], v[226:229], v[0:3]
	v_mfma_f32_16x16x32_bf16 v[28:31], v[174:177], v[206:209], v[28:31]
	v_mfma_f32_16x16x32_bf16 v[24:27], v[182:185], v[206:209], v[24:27]
	v_mfma_f32_16x16x32_bf16 v[20:23], v[174:177], v[214:217], v[20:23]
	v_mfma_f32_16x16x32_bf16 v[16:19], v[182:185], v[214:217], v[16:19]
	v_mfma_f32_16x16x32_bf16 v[12:15], v[174:177], v[222:225], v[12:15]
	v_mfma_f32_16x16x32_bf16 v[8:11], v[182:185], v[222:225], v[8:11]
	v_mfma_f32_16x16x32_bf16 v[4:7], v[174:177], v[230:233], v[4:7]
	v_mfma_f32_16x16x32_bf16 v[0:3], v[182:185], v[230:233], v[0:3]
	s_setprio 0
	s_setprio 1
	v_mfma_f32_16x16x32_bf16 v[92:95], v[186:189], v[202:205], v[92:95]
	v_mfma_f32_16x16x32_bf16 v[88:91], v[194:197], v[202:205], v[88:91]
	v_mfma_f32_16x16x32_bf16 v[84:87], v[186:189], v[210:213], v[84:87]
	v_mfma_f32_16x16x32_bf16 v[80:83], v[194:197], v[210:213], v[80:83]
	v_mfma_f32_16x16x32_bf16 v[72:75], v[186:189], v[218:221], v[72:75]
	v_mfma_f32_16x16x32_bf16 v[76:79], v[194:197], v[218:221], v[76:79]
	v_mfma_f32_16x16x32_bf16 v[64:67], v[186:189], v[226:229], v[64:67]
	v_mfma_f32_16x16x32_bf16 v[68:71], v[194:197], v[226:229], v[68:71]
	v_mfma_f32_16x16x32_bf16 v[92:95], v[190:193], v[206:209], v[92:95]
	v_mfma_f32_16x16x32_bf16 v[88:91], v[198:201], v[206:209], v[88:91]
	v_mfma_f32_16x16x32_bf16 v[84:87], v[190:193], v[214:217], v[84:87]
	v_mfma_f32_16x16x32_bf16 v[80:83], v[198:201], v[214:217], v[80:83]
	v_mfma_f32_16x16x32_bf16 v[72:75], v[190:193], v[222:225], v[72:75]
	v_mfma_f32_16x16x32_bf16 v[76:79], v[198:201], v[222:225], v[76:79]
	v_mfma_f32_16x16x32_bf16 v[64:67], v[190:193], v[230:233], v[64:67]
	v_mfma_f32_16x16x32_bf16 v[68:71], v[198:201], v[230:233], v[68:71]
	s_setprio 0
	s_barrier
	s_add_i32 s71, 0, 0x18000
	v_add_u32_e32 v133, s71, v161
	s_add_i32 s72, 0, 0x1c000
	ds_read_b128 v[170:173], v133
	ds_read_b128 v[174:177], v133 offset:1024
	ds_read_b128 v[178:181], v133 offset:2048
	ds_read_b128 v[182:185], v133 offset:3072
	v_add_u32_e32 v133, s72, v161
	ds_read_b128 v[186:189], v133
	ds_read_b128 v[190:193], v133 offset:1024
	ds_read_b128 v[194:197], v133 offset:2048
	ds_read_b128 v[198:201], v133 offset:3072
	s_mov_b32 m0, s9
	ds_read_b128 v[202:205], v165 offset:32768
	ds_read_b128 v[206:209], v165 offset:33792
	ds_read_b128 v[210:213], v165 offset:34816
	ds_read_b128 v[214:217], v165 offset:35840
	ds_read_b128 v[218:221], v165 offset:36864
	ds_read_b128 v[222:225], v165 offset:37888
	ds_read_b128 v[226:229], v165 offset:38912
	ds_read_b128 v[230:233], v165 offset:39936
	global_load_lds_dwordx4 v129, s[54:55]
	s_mov_b32 m0, s31
	s_nop 0
	global_load_lds_dwordx4 v131, s[54:55]
	s_waitcnt vmcnt(8)
	s_waitcnt lgkmcnt(0)
	s_barrier
	s_setprio 1
	v_mfma_f32_16x16x32_bf16 v[60:63], v[170:173], v[202:205], v[60:63]
	v_mfma_f32_16x16x32_bf16 v[56:59], v[178:181], v[202:205], v[56:59]
	v_mfma_f32_16x16x32_bf16 v[52:55], v[170:173], v[210:213], v[52:55]
	v_mfma_f32_16x16x32_bf16 v[48:51], v[178:181], v[210:213], v[48:51]
	v_mfma_f32_16x16x32_bf16 v[44:47], v[170:173], v[218:221], v[44:47]
	v_mfma_f32_16x16x32_bf16 v[40:43], v[178:181], v[218:221], v[40:43]
	v_mfma_f32_16x16x32_bf16 v[36:39], v[170:173], v[226:229], v[36:39]
	v_mfma_f32_16x16x32_bf16 v[32:35], v[178:181], v[226:229], v[32:35]
	v_mfma_f32_16x16x32_bf16 v[60:63], v[174:177], v[206:209], v[60:63]
	v_mfma_f32_16x16x32_bf16 v[56:59], v[182:185], v[206:209], v[56:59]
	v_mfma_f32_16x16x32_bf16 v[52:55], v[174:177], v[214:217], v[52:55]
	v_mfma_f32_16x16x32_bf16 v[48:51], v[182:185], v[214:217], v[48:51]
	v_mfma_f32_16x16x32_bf16 v[44:47], v[174:177], v[222:225], v[44:47]
	v_mfma_f32_16x16x32_bf16 v[40:43], v[182:185], v[222:225], v[40:43]
	v_mfma_f32_16x16x32_bf16 v[36:39], v[174:177], v[230:233], v[36:39]
	v_mfma_f32_16x16x32_bf16 v[32:35], v[182:185], v[230:233], v[32:35]
	s_setprio 0
	s_setprio 1
	v_mfma_f32_16x16x32_bf16 v[124:127], v[186:189], v[202:205], v[124:127]
	v_mfma_f32_16x16x32_bf16 v[120:123], v[194:197], v[202:205], v[120:123]
	v_mfma_f32_16x16x32_bf16 v[116:119], v[186:189], v[210:213], v[116:119]
	v_mfma_f32_16x16x32_bf16 v[112:115], v[194:197], v[210:213], v[112:115]
	v_mfma_f32_16x16x32_bf16 v[108:111], v[186:189], v[218:221], v[108:111]
	v_mfma_f32_16x16x32_bf16 v[104:107], v[194:197], v[218:221], v[104:107]
	v_mfma_f32_16x16x32_bf16 v[100:103], v[186:189], v[226:229], v[100:103]
	v_mfma_f32_16x16x32_bf16 v[96:99], v[194:197], v[226:229], v[96:99]
	v_mfma_f32_16x16x32_bf16 v[124:127], v[190:193], v[206:209], v[124:127]
	v_mfma_f32_16x16x32_bf16 v[120:123], v[198:201], v[206:209], v[120:123]
	v_mfma_f32_16x16x32_bf16 v[116:119], v[190:193], v[214:217], v[116:119]
	v_mfma_f32_16x16x32_bf16 v[112:115], v[198:201], v[214:217], v[112:115]
	v_mfma_f32_16x16x32_bf16 v[108:111], v[190:193], v[222:225], v[108:111]
	v_mfma_f32_16x16x32_bf16 v[104:107], v[198:201], v[222:225], v[104:107]
	v_mfma_f32_16x16x32_bf16 v[100:103], v[190:193], v[230:233], v[100:103]
	v_mfma_f32_16x16x32_bf16 v[96:99], v[198:201], v[230:233], v[96:99]
	s_setprio 0
	s_barrier
	s_add_i32 s54, s71, s0
	v_lshl_add_u64 v[234:235], v[234:235], 0, s[24:25]
	s_mov_b32 m0, s54
	ds_read_b128 v[202:205], v165 offset:49152
	ds_read_b128 v[206:209], v165 offset:50176
	ds_read_b128 v[210:213], v165 offset:51200
	ds_read_b128 v[214:217], v165 offset:52224
	ds_read_b128 v[218:221], v165 offset:53248
	ds_read_b128 v[222:225], v165 offset:54272
	ds_read_b128 v[226:229], v165 offset:55296
	ds_read_b128 v[230:233], v165 offset:56320
	global_load_lds_dwordx4 v[234:235], off
	s_add_i32 m0, s54, 0x2000
	s_add_u32 s52, s52, 0x80080
	v_lshl_add_u64 v[234:235], v[236:237], 0, s[24:25]
	s_addc_u32 s53, s53, 0
	s_add_i32 s54, s72, s0
	global_load_lds_dwordx4 v[234:235], off
	v_lshl_add_u64 v[234:235], s[52:53], 0, v[136:137]
	s_mov_b32 m0, s54
	v_lshl_add_u64 v[154:155], v[154:155], 0, s[24:25]
	global_load_lds_dwordx4 v[234:235], off
	v_lshl_add_u64 v[234:235], s[52:53], 0, v[138:139]
	s_add_i32 m0, s54, 0x2000
	s_nop 0
	global_load_lds_dwordx4 v[234:235], off
	v_lshl_add_u64 v[234:235], v[238:239], 0, s[24:25]
	s_mov_b32 m0, s60
	s_nop 0
	global_load_lds_dwordx4 v[234:235], off
	s_mov_b32 m0, s61
	s_nop 0
	global_load_lds_dwordx4 v[154:155], off
	s_waitcnt vmcnt(8)
	s_waitcnt lgkmcnt(0)
	s_barrier
	s_setprio 1
	v_mfma_f32_16x16x32_bf16 v[28:31], v[170:173], v[202:205], v[28:31]
	v_mfma_f32_16x16x32_bf16 v[24:27], v[178:181], v[202:205], v[24:27]
	v_mfma_f32_16x16x32_bf16 v[20:23], v[170:173], v[210:213], v[20:23]
	v_mfma_f32_16x16x32_bf16 v[16:19], v[178:181], v[210:213], v[16:19]
	v_mfma_f32_16x16x32_bf16 v[12:15], v[170:173], v[218:221], v[12:15]
	v_mfma_f32_16x16x32_bf16 v[8:11], v[178:181], v[218:221], v[8:11]
	v_mfma_f32_16x16x32_bf16 v[4:7], v[170:173], v[226:229], v[4:7]
	v_mfma_f32_16x16x32_bf16 v[0:3], v[178:181], v[226:229], v[0:3]
	v_mfma_f32_16x16x32_bf16 v[28:31], v[174:177], v[206:209], v[28:31]
	v_mfma_f32_16x16x32_bf16 v[24:27], v[182:185], v[206:209], v[24:27]
	v_mfma_f32_16x16x32_bf16 v[20:23], v[174:177], v[214:217], v[20:23]
	v_mfma_f32_16x16x32_bf16 v[16:19], v[182:185], v[214:217], v[16:19]
	v_mfma_f32_16x16x32_bf16 v[12:15], v[174:177], v[222:225], v[12:15]
	v_mfma_f32_16x16x32_bf16 v[8:11], v[182:185], v[222:225], v[8:11]
	v_mfma_f32_16x16x32_bf16 v[4:7], v[174:177], v[230:233], v[4:7]
	v_mfma_f32_16x16x32_bf16 v[0:3], v[182:185], v[230:233], v[0:3]
	s_setprio 0
	s_setprio 1
	v_mfma_f32_16x16x32_bf16 v[92:95], v[186:189], v[202:205], v[92:95]
	v_mfma_f32_16x16x32_bf16 v[88:91], v[194:197], v[202:205], v[88:91]
	v_mfma_f32_16x16x32_bf16 v[84:87], v[186:189], v[210:213], v[84:87]
	v_mfma_f32_16x16x32_bf16 v[80:83], v[194:197], v[210:213], v[80:83]
	v_mfma_f32_16x16x32_bf16 v[72:75], v[186:189], v[218:221], v[72:75]
	v_mfma_f32_16x16x32_bf16 v[76:79], v[194:197], v[218:221], v[76:79]
	v_mfma_f32_16x16x32_bf16 v[64:67], v[186:189], v[226:229], v[64:67]
	v_mfma_f32_16x16x32_bf16 v[68:71], v[194:197], v[226:229], v[68:71]
	v_mfma_f32_16x16x32_bf16 v[92:95], v[190:193], v[206:209], v[92:95]
	v_mfma_f32_16x16x32_bf16 v[88:91], v[198:201], v[206:209], v[88:91]
	v_mfma_f32_16x16x32_bf16 v[84:87], v[190:193], v[214:217], v[84:87]
	v_mfma_f32_16x16x32_bf16 v[80:83], v[198:201], v[214:217], v[80:83]
	v_mfma_f32_16x16x32_bf16 v[72:75], v[190:193], v[222:225], v[72:75]
	v_mfma_f32_16x16x32_bf16 v[76:79], v[198:201], v[222:225], v[76:79]
	v_mfma_f32_16x16x32_bf16 v[64:67], v[190:193], v[230:233], v[64:67]
	v_mfma_f32_16x16x32_bf16 v[68:71], v[198:201], v[230:233], v[68:71]
	s_setprio 0
	s_barrier
	s_add_i32 s70, s70, 2
	s_add_u32 s4, s4, 0x100
	s_addc_u32 s5, s5, 0
	s_cmp_gt_u32 s70, 29
	s_cbranch_scc0 .LBB0_180
	s_and_b64 vcc, exec, s[26:27]
	s_cbranch_vccnz .LBB0_184
	v_lshl_add_u32 v150, s62, 8, v160
	s_cmp_lg_u32 s6, 46
	s_mov_b64 s[4:5], -1
	s_cbranch_scc1 .LBB0_185

.LBB0_888:
	s_add_i32 s63, s38, 2
	s_add_u32 s39, s30, s36
	s_addc_u32 s40, s31, s37
	v_add_u32_e32 v131, s44, v152
	s_add_u32 s64, s39, 0x100
	ds_read_b128 v[160:163], v131
	ds_read_b128 v[164:167], v131 offset:1024
	ds_read_b128 v[168:171], v131 offset:2048
	ds_read_b128 v[172:175], v131 offset:3072
	v_add_u32_e32 v131, s45, v152
	s_addc_u32 s40, s40, 0
	ds_read_b128 v[176:179], v131
	ds_read_b128 v[180:183], v131 offset:1024
	ds_read_b128 v[184:187], v131 offset:2048
	ds_read_b128 v[188:191], v131 offset:3072
	s_add_u32 s65, s61, s36
	s_addc_u32 s66, s62, s37
	s_cmp_eq_u32 s60, s38
	s_cselect_b64 vcc, -1, 0
	s_and_b64 s[38:39], vcc, exec
	s_cselect_b32 s38, s55, s65
	v_cndmask_b32_e32 v136, v128, v156, vcc
	s_cselect_b32 s41, s57, s40
	s_cselect_b32 s40, s59, s64
	v_cndmask_b32_e32 v129, v138, v158, vcc
	v_cndmask_b32_e32 v224, v130, v157, vcc
	v_cndmask_b32_e32 v131, v140, v159, vcc
	s_cselect_b32 s39, s25, s66
	v_lshl_add_u64 v[226:227], v[146:147], 0, s[36:37]
	s_add_i32 m0, s1, 0xc000
	ds_read_b128 v[192:195], v155
	ds_read_b128 v[196:199], v155 offset:1024
	ds_read_b128 v[200:203], v155 offset:2048
	ds_read_b128 v[204:207], v155 offset:3072
	ds_read_b128 v[208:211], v155 offset:4096
	ds_read_b128 v[212:215], v155 offset:5120
	ds_read_b128 v[216:219], v155 offset:6144
	ds_read_b128 v[220:223], v155 offset:7168
	global_load_lds_dwordx4 v[226:227], off
	v_lshl_add_u64 v[226:227], v[142:143], 0, s[36:37]
	s_add_i32 m0, s1, 0xe000
	s_nop 0
	global_load_lds_dwordx4 v[226:227], off
	s_waitcnt vmcnt(8)
	s_waitcnt lgkmcnt(0)
	s_barrier
	s_setprio 1
	v_mfma_f32_16x16x32_bf16 v[108:111], v[160:163], v[192:195], v[108:111]
	v_mfma_f32_16x16x32_bf16 v[104:107], v[168:171], v[192:195], v[104:107]
	v_mfma_f32_16x16x32_bf16 v[100:103], v[160:163], v[200:203], v[100:103]
	v_mfma_f32_16x16x32_bf16 v[96:99], v[168:171], v[200:203], v[96:99]
	v_mfma_f32_16x16x32_bf16 v[92:95], v[160:163], v[208:211], v[92:95]
	v_mfma_f32_16x16x32_bf16 v[88:91], v[168:171], v[208:211], v[88:91]
	v_mfma_f32_16x16x32_bf16 v[84:87], v[160:163], v[216:219], v[84:87]
	v_mfma_f32_16x16x32_bf16 v[80:83], v[168:171], v[216:219], v[80:83]
	v_mfma_f32_16x16x32_bf16 v[108:111], v[164:167], v[196:199], v[108:111]
	v_mfma_f32_16x16x32_bf16 v[104:107], v[172:175], v[196:199], v[104:107]
	v_mfma_f32_16x16x32_bf16 v[100:103], v[164:167], v[204:207], v[100:103]
	v_mfma_f32_16x16x32_bf16 v[96:99], v[172:175], v[204:207], v[96:99]
	v_mfma_f32_16x16x32_bf16 v[92:95], v[164:167], v[212:215], v[92:95]
	v_mfma_f32_16x16x32_bf16 v[88:91], v[172:175], v[212:215], v[88:91]
	v_mfma_f32_16x16x32_bf16 v[84:87], v[164:167], v[220:223], v[84:87]
	v_mfma_f32_16x16x32_bf16 v[80:83], v[172:175], v[220:223], v[80:83]
	s_setprio 0
	s_setprio 1
	v_mfma_f32_16x16x32_bf16 v[76:79], v[176:179], v[192:195], v[76:79]
	v_mfma_f32_16x16x32_bf16 v[72:75], v[184:187], v[192:195], v[72:75]
	v_mfma_f32_16x16x32_bf16 v[68:71], v[176:179], v[200:203], v[68:71]
	v_mfma_f32_16x16x32_bf16 v[64:67], v[184:187], v[200:203], v[64:67]
	v_mfma_f32_16x16x32_bf16 v[60:63], v[176:179], v[208:211], v[60:63]
	v_mfma_f32_16x16x32_bf16 v[56:59], v[184:187], v[208:211], v[56:59]
	v_mfma_f32_16x16x32_bf16 v[52:55], v[176:179], v[216:219], v[52:55]
	v_mfma_f32_16x16x32_bf16 v[48:51], v[184:187], v[216:219], v[48:51]
	v_mfma_f32_16x16x32_bf16 v[76:79], v[180:183], v[196:199], v[76:79]
	v_mfma_f32_16x16x32_bf16 v[72:75], v[188:191], v[196:199], v[72:75]
	v_mfma_f32_16x16x32_bf16 v[68:71], v[180:183], v[204:207], v[68:71]
	v_mfma_f32_16x16x32_bf16 v[64:67], v[188:191], v[204:207], v[64:67]
	v_mfma_f32_16x16x32_bf16 v[60:63], v[180:183], v[212:215], v[60:63]
	v_mfma_f32_16x16x32_bf16 v[56:59], v[188:191], v[212:215], v[56:59]
	v_mfma_f32_16x16x32_bf16 v[52:55], v[180:183], v[220:223], v[52:55]
	v_mfma_f32_16x16x32_bf16 v[48:51], v[188:191], v[220:223], v[48:51]
	s_setprio 0
	s_barrier
	s_add_i32 s64, s44, s0
	v_lshl_add_u64 v[226:227], s[38:39], 0, v[132:133]
	s_mov_b32 m0, s64
	ds_read_b128 v[192:195], v155 offset:16384
	ds_read_b128 v[196:199], v155 offset:17408
	ds_read_b128 v[200:203], v155 offset:18432
	ds_read_b128 v[204:207], v155 offset:19456
	ds_read_b128 v[208:211], v155 offset:20480
	ds_read_b128 v[212:215], v155 offset:21504
	ds_read_b128 v[216:219], v155 offset:22528
	ds_read_b128 v[220:223], v155 offset:23552
	global_load_lds_dwordx4 v[226:227], off
	s_add_i32 m0, s64, 0x2000
	s_add_u32 s64, s38, 0x80000
	v_lshl_add_u64 v[228:229], s[38:39], 0, v[134:135]
	s_addc_u32 s65, s39, 0
	s_add_i32 s66, s45, s0
	global_load_lds_dwordx4 v[228:229], off
	v_lshl_add_u64 v[230:231], s[64:65], 0, v[132:133]
	s_mov_b32 m0, s66
	v_mov_b32_e32 v225, v137
	global_load_lds_dwordx4 v[230:231], off
	v_lshl_add_u64 v[230:231], s[64:65], 0, v[134:135]
	s_add_i32 m0, s66, 0x2000
	s_nop 0
	global_load_lds_dwordx4 v[230:231], off
	s_mov_b32 m0, s1
	v_lshl_add_u64 v[230:231], s[40:41], 0, v[136:137]
	global_load_lds_dwordx4 v136, s[40:41]
	s_mov_b32 m0, s4
	s_nop 0
	global_load_lds_dwordx4 v224, s[40:41]
	s_waitcnt vmcnt(8)
	s_waitcnt lgkmcnt(0)
	v_lshl_add_u64 v[224:225], s[40:41], 0, v[224:225]
	s_barrier
	s_setprio 1
	v_mfma_f32_16x16x32_bf16 v[44:47], v[160:163], v[192:195], v[44:47]
	v_mfma_f32_16x16x32_bf16 v[40:43], v[168:171], v[192:195], v[40:43]
	v_mfma_f32_16x16x32_bf16 v[36:39], v[160:163], v[200:203], v[36:39]
	v_mfma_f32_16x16x32_bf16 v[32:35], v[168:171], v[200:203], v[32:35]
	v_mfma_f32_16x16x32_bf16 v[28:31], v[160:163], v[208:211], v[28:31]
	v_mfma_f32_16x16x32_bf16 v[24:27], v[168:171], v[208:211], v[24:27]
	v_mfma_f32_16x16x32_bf16 v[20:23], v[160:163], v[216:219], v[20:23]
	v_mfma_f32_16x16x32_bf16 v[16:19], v[168:171], v[216:219], v[16:19]
	v_mfma_f32_16x16x32_bf16 v[44:47], v[164:167], v[196:199], v[44:47]
	v_mfma_f32_16x16x32_bf16 v[40:43], v[172:175], v[196:199], v[40:43]
	v_mfma_f32_16x16x32_bf16 v[36:39], v[164:167], v[204:207], v[36:39]
	v_mfma_f32_16x16x32_bf16 v[32:35], v[172:175], v[204:207], v[32:35]
	v_mfma_f32_16x16x32_bf16 v[28:31], v[164:167], v[212:215], v[28:31]
	v_mfma_f32_16x16x32_bf16 v[24:27], v[172:175], v[212:215], v[24:27]
	v_mfma_f32_16x16x32_bf16 v[20:23], v[164:167], v[220:223], v[20:23]
	v_mfma_f32_16x16x32_bf16 v[16:19], v[172:175], v[220:223], v[16:19]
	s_setprio 0
	s_setprio 1
	v_mfma_f32_16x16x32_bf16 v[12:15], v[176:179], v[192:195], v[12:15]
	v_mfma_f32_16x16x32_bf16 v[8:11], v[184:187], v[192:195], v[8:11]
	v_mfma_f32_16x16x32_bf16 v[4:7], v[176:179], v[200:203], v[4:7]
	v_mfma_f32_16x16x32_bf16 v[0:3], v[184:187], v[200:203], v[0:3]
	v_mfma_f32_16x16x32_bf16 v[112:115], v[176:179], v[208:211], v[112:115]
	v_mfma_f32_16x16x32_bf16 v[116:119], v[184:187], v[208:211], v[116:119]
	v_mfma_f32_16x16x32_bf16 v[120:123], v[176:179], v[216:219], v[120:123]
	v_mfma_f32_16x16x32_bf16 v[124:127], v[184:187], v[216:219], v[124:127]
	v_mfma_f32_16x16x32_bf16 v[12:15], v[180:183], v[196:199], v[12:15]
	v_mfma_f32_16x16x32_bf16 v[8:11], v[188:191], v[196:199], v[8:11]
	v_mfma_f32_16x16x32_bf16 v[4:7], v[180:183], v[204:207], v[4:7]
	v_mfma_f32_16x16x32_bf16 v[0:3], v[188:191], v[204:207], v[0:3]
	v_mfma_f32_16x16x32_bf16 v[112:115], v[180:183], v[212:215], v[112:115]
	v_mfma_f32_16x16x32_bf16 v[116:119], v[188:191], v[212:215], v[116:119]
	v_mfma_f32_16x16x32_bf16 v[120:123], v[180:183], v[220:223], v[120:123]
	v_mfma_f32_16x16x32_bf16 v[124:127], v[188:191], v[220:223], v[124:127]
	s_setprio 0
	s_barrier
	s_add_i32 s64, 0, 0x18000
	v_add_u32_e32 v136, s64, v152
	s_add_i32 s65, 0, 0x1c000
	ds_read_b128 v[160:163], v136
	ds_read_b128 v[164:167], v136 offset:1024
	ds_read_b128 v[168:171], v136 offset:2048
	ds_read_b128 v[172:175], v136 offset:3072
	v_add_u32_e32 v136, s65, v152
	ds_read_b128 v[176:179], v136
	ds_read_b128 v[180:183], v136 offset:1024
	ds_read_b128 v[184:187], v136 offset:2048
	ds_read_b128 v[188:191], v136 offset:3072
	s_mov_b32 m0, s5
	ds_read_b128 v[192:195], v155 offset:32768
	ds_read_b128 v[196:199], v155 offset:33792
	ds_read_b128 v[200:203], v155 offset:34816
	ds_read_b128 v[204:207], v155 offset:35840
	ds_read_b128 v[208:211], v155 offset:36864
	ds_read_b128 v[212:215], v155 offset:37888
	ds_read_b128 v[216:219], v155 offset:38912
	ds_read_b128 v[220:223], v155 offset:39936
	global_load_lds_dwordx4 v129, s[40:41]
	s_mov_b32 m0, s6
	s_nop 0
	global_load_lds_dwordx4 v131, s[40:41]
	s_waitcnt vmcnt(8)
	s_waitcnt lgkmcnt(0)
	s_barrier
	s_setprio 1
	v_mfma_f32_16x16x32_bf16 v[108:111], v[160:163], v[192:195], v[108:111]
	v_mfma_f32_16x16x32_bf16 v[104:107], v[168:171], v[192:195], v[104:107]
	v_mfma_f32_16x16x32_bf16 v[100:103], v[160:163], v[200:203], v[100:103]
	v_mfma_f32_16x16x32_bf16 v[96:99], v[168:171], v[200:203], v[96:99]
	v_mfma_f32_16x16x32_bf16 v[92:95], v[160:163], v[208:211], v[92:95]
	v_mfma_f32_16x16x32_bf16 v[88:91], v[168:171], v[208:211], v[88:91]
	v_mfma_f32_16x16x32_bf16 v[84:87], v[160:163], v[216:219], v[84:87]
	v_mfma_f32_16x16x32_bf16 v[80:83], v[168:171], v[216:219], v[80:83]
	v_mfma_f32_16x16x32_bf16 v[108:111], v[164:167], v[196:199], v[108:111]
	v_mfma_f32_16x16x32_bf16 v[104:107], v[172:175], v[196:199], v[104:107]
	v_mfma_f32_16x16x32_bf16 v[100:103], v[164:167], v[204:207], v[100:103]
	v_mfma_f32_16x16x32_bf16 v[96:99], v[172:175], v[204:207], v[96:99]
	v_mfma_f32_16x16x32_bf16 v[92:95], v[164:167], v[212:215], v[92:95]
	v_mfma_f32_16x16x32_bf16 v[88:91], v[172:175], v[212:215], v[88:91]
	v_mfma_f32_16x16x32_bf16 v[84:87], v[164:167], v[220:223], v[84:87]
	v_mfma_f32_16x16x32_bf16 v[80:83], v[172:175], v[220:223], v[80:83]
	s_setprio 0
	s_setprio 1
	v_mfma_f32_16x16x32_bf16 v[76:79], v[176:179], v[192:195], v[76:79]
	v_mfma_f32_16x16x32_bf16 v[72:75], v[184:187], v[192:195], v[72:75]
	v_mfma_f32_16x16x32_bf16 v[68:71], v[176:179], v[200:203], v[68:71]
	v_mfma_f32_16x16x32_bf16 v[64:67], v[184:187], v[200:203], v[64:67]
	v_mfma_f32_16x16x32_bf16 v[60:63], v[176:179], v[208:211], v[60:63]
	v_mfma_f32_16x16x32_bf16 v[56:59], v[184:187], v[208:211], v[56:59]
	v_mfma_f32_16x16x32_bf16 v[52:55], v[176:179], v[216:219], v[52:55]
	v_mfma_f32_16x16x32_bf16 v[48:51], v[184:187], v[216:219], v[48:51]
	v_mfma_f32_16x16x32_bf16 v[76:79], v[180:183], v[196:199], v[76:79]
	v_mfma_f32_16x16x32_bf16 v[72:75], v[188:191], v[196:199], v[72:75]
	v_mfma_f32_16x16x32_bf16 v[68:71], v[180:183], v[204:207], v[68:71]
	v_mfma_f32_16x16x32_bf16 v[64:67], v[188:191], v[204:207], v[64:67]
	v_mfma_f32_16x16x32_bf16 v[60:63], v[180:183], v[212:215], v[60:63]
	v_mfma_f32_16x16x32_bf16 v[56:59], v[188:191], v[212:215], v[56:59]
	v_mfma_f32_16x16x32_bf16 v[52:55], v[180:183], v[220:223], v[52:55]
	v_mfma_f32_16x16x32_bf16 v[48:51], v[188:191], v[220:223], v[48:51]
	s_setprio 0
	s_barrier
	s_add_i32 s40, s64, s0
	v_lshl_add_u64 v[226:227], v[226:227], 0, s[18:19]
	s_mov_b32 m0, s40
	ds_read_b128 v[192:195], v155 offset:49152
	ds_read_b128 v[196:199], v155 offset:50176
	ds_read_b128 v[200:203], v155 offset:51200
	ds_read_b128 v[204:207], v155 offset:52224
	ds_read_b128 v[208:211], v155 offset:53248
	ds_read_b128 v[212:215], v155 offset:54272
	ds_read_b128 v[216:219], v155 offset:55296
	ds_read_b128 v[220:223], v155 offset:56320
	global_load_lds_dwordx4 v[226:227], off
	s_add_i32 m0, s40, 0x2000
	s_add_u32 s38, s38, 0x80080
	v_lshl_add_u64 v[226:227], v[228:229], 0, s[18:19]
	s_addc_u32 s39, s39, 0
	s_add_i32 s40, s65, s0
	global_load_lds_dwordx4 v[226:227], off
	v_lshl_add_u64 v[226:227], s[38:39], 0, v[132:133]
	s_mov_b32 m0, s40
	v_lshl_add_u64 v[224:225], v[224:225], 0, s[18:19]
	global_load_lds_dwordx4 v[226:227], off
	v_lshl_add_u64 v[226:227], s[38:39], 0, v[134:135]
	s_add_i32 m0, s40, 0x2000
	s_nop 0
	global_load_lds_dwordx4 v[226:227], off
	v_lshl_add_u64 v[226:227], v[230:231], 0, s[18:19]
	s_mov_b32 m0, s9
	s_nop 0
	global_load_lds_dwordx4 v[226:227], off
	s_mov_b32 m0, s42
	s_nop 0
	global_load_lds_dwordx4 v[224:225], off
	s_waitcnt vmcnt(8)
	s_waitcnt lgkmcnt(0)
	s_barrier
	s_setprio 1
	v_mfma_f32_16x16x32_bf16 v[44:47], v[160:163], v[192:195], v[44:47]
	v_mfma_f32_16x16x32_bf16 v[40:43], v[168:171], v[192:195], v[40:43]
	v_mfma_f32_16x16x32_bf16 v[36:39], v[160:163], v[200:203], v[36:39]
	v_mfma_f32_16x16x32_bf16 v[32:35], v[168:171], v[200:203], v[32:35]
	v_mfma_f32_16x16x32_bf16 v[28:31], v[160:163], v[208:211], v[28:31]
	v_mfma_f32_16x16x32_bf16 v[24:27], v[168:171], v[208:211], v[24:27]
	v_mfma_f32_16x16x32_bf16 v[20:23], v[160:163], v[216:219], v[20:23]
	v_mfma_f32_16x16x32_bf16 v[16:19], v[168:171], v[216:219], v[16:19]
	v_mfma_f32_16x16x32_bf16 v[44:47], v[164:167], v[196:199], v[44:47]
	v_mfma_f32_16x16x32_bf16 v[40:43], v[172:175], v[196:199], v[40:43]
	v_mfma_f32_16x16x32_bf16 v[36:39], v[164:167], v[204:207], v[36:39]
	v_mfma_f32_16x16x32_bf16 v[32:35], v[172:175], v[204:207], v[32:35]
	v_mfma_f32_16x16x32_bf16 v[28:31], v[164:167], v[212:215], v[28:31]
	v_mfma_f32_16x16x32_bf16 v[24:27], v[172:175], v[212:215], v[24:27]
	v_mfma_f32_16x16x32_bf16 v[20:23], v[164:167], v[220:223], v[20:23]
	v_mfma_f32_16x16x32_bf16 v[16:19], v[172:175], v[220:223], v[16:19]
	s_setprio 0
	s_setprio 1
	v_mfma_f32_16x16x32_bf16 v[12:15], v[176:179], v[192:195], v[12:15]
	v_mfma_f32_16x16x32_bf16 v[8:11], v[184:187], v[192:195], v[8:11]
	v_mfma_f32_16x16x32_bf16 v[4:7], v[176:179], v[200:203], v[4:7]
	v_mfma_f32_16x16x32_bf16 v[0:3], v[184:187], v[200:203], v[0:3]
	v_mfma_f32_16x16x32_bf16 v[112:115], v[176:179], v[208:211], v[112:115]
	v_mfma_f32_16x16x32_bf16 v[116:119], v[184:187], v[208:211], v[116:119]
	v_mfma_f32_16x16x32_bf16 v[120:123], v[176:179], v[216:219], v[120:123]
	v_mfma_f32_16x16x32_bf16 v[124:127], v[184:187], v[216:219], v[124:127]
	v_mfma_f32_16x16x32_bf16 v[12:15], v[180:183], v[196:199], v[12:15]
	v_mfma_f32_16x16x32_bf16 v[8:11], v[188:191], v[196:199], v[8:11]
	v_mfma_f32_16x16x32_bf16 v[4:7], v[180:183], v[204:207], v[4:7]
	v_mfma_f32_16x16x32_bf16 v[0:3], v[188:191], v[204:207], v[0:3]
	v_mfma_f32_16x16x32_bf16 v[112:115], v[180:183], v[212:215], v[112:115]
	v_mfma_f32_16x16x32_bf16 v[116:119], v[188:191], v[212:215], v[116:119]
	v_mfma_f32_16x16x32_bf16 v[120:123], v[180:183], v[220:223], v[120:123]
	v_mfma_f32_16x16x32_bf16 v[124:127], v[188:191], v[220:223], v[124:127]
	s_setprio 0
	s_barrier
	s_add_u32 s36, s36, 0x100
	s_addc_u32 s37, s37, 0
	s_cmp_ge_i32 s63, s53
	s_mov_b32 s38, s63
	s_cbranch_scc0 .LBB0_888
	s_and_b64 vcc, exec, s[20:21]
	s_cbranch_vccz .LBB0_891
	s_barrier

.LBB0_964:
	ds_read_b128 v[140:143], v162
	ds_read_b128 v[170:173], v162 offset:1024
	ds_read_b128 v[174:177], v162 offset:2048
	ds_read_b128 v[178:181], v162 offset:3072
	ds_read_b128 v[182:185], v163
	ds_read_b128 v[186:189], v163 offset:1024
	ds_read_b128 v[190:193], v163 offset:2048
	ds_read_b128 v[194:197], v163 offset:3072
	s_add_u32 s46, s42, s12
	s_addc_u32 s47, s43, s13
	s_cmpk_eq_i32 s12, 0x1000
	s_cselect_b64 vcc, -1, 0
	s_and_b64 s[44:45], vcc, exec
	s_cselect_b32 s64, 0, s12
	s_cselect_b32 s63, 0, s13
	s_cselect_b32 s44, s61, s46
	s_cselect_b32 s45, s39, s47
	s_add_u32 s46, s14, s64
	v_cndmask_b32_e32 v150, v128, v165, vcc
	v_cndmask_b32_e32 v129, v132, v167, vcc
	v_cndmask_b32_e32 v230, v130, v166, vcc
	v_cndmask_b32_e32 v131, v134, v168, vcc
	s_addc_u32 s47, s15, s63
	v_lshl_add_u64 v[232:233], v[138:139], 0, s[12:13]
	v_lshl_add_u64 v[232:233], v[232:233], 0, s[28:29]
	s_add_i32 m0, s4, 0xc000
	ds_read_b128 v[198:201], v164
	ds_read_b128 v[202:205], v164 offset:1024
	ds_read_b128 v[206:209], v164 offset:2048
	ds_read_b128 v[210:213], v164 offset:3072
	ds_read_b128 v[214:217], v164 offset:4096
	ds_read_b128 v[218:221], v164 offset:5120
	ds_read_b128 v[222:225], v164 offset:6144
	ds_read_b128 v[226:229], v164 offset:7168
	global_load_lds_dwordx4 v[232:233], off
	v_lshl_add_u64 v[232:233], v[136:137], 0, s[12:13]
	v_lshl_add_u64 v[232:233], v[232:233], 0, s[28:29]
	s_add_i32 m0, s4, 0xe000
	s_nop 0
	global_load_lds_dwordx4 v[232:233], off
	s_waitcnt vmcnt(8)
	s_waitcnt lgkmcnt(0)
	s_barrier
	s_setprio 1
	v_mfma_f32_16x16x32_bf16 v[124:127], v[140:143], v[198:201], v[124:127]
	v_mfma_f32_16x16x32_bf16 v[120:123], v[174:177], v[198:201], v[120:123]
	v_mfma_f32_16x16x32_bf16 v[116:119], v[140:143], v[206:209], v[116:119]
	v_mfma_f32_16x16x32_bf16 v[112:115], v[174:177], v[206:209], v[112:115]
	v_mfma_f32_16x16x32_bf16 v[108:111], v[140:143], v[214:217], v[108:111]
	v_mfma_f32_16x16x32_bf16 v[100:103], v[174:177], v[214:217], v[100:103]
	v_mfma_f32_16x16x32_bf16 v[92:95], v[140:143], v[222:225], v[92:95]
	v_mfma_f32_16x16x32_bf16 v[84:87], v[174:177], v[222:225], v[84:87]
	v_mfma_f32_16x16x32_bf16 v[124:127], v[170:173], v[202:205], v[124:127]
	v_mfma_f32_16x16x32_bf16 v[120:123], v[178:181], v[202:205], v[120:123]
	v_mfma_f32_16x16x32_bf16 v[116:119], v[170:173], v[210:213], v[116:119]
	v_mfma_f32_16x16x32_bf16 v[112:115], v[178:181], v[210:213], v[112:115]
	v_mfma_f32_16x16x32_bf16 v[108:111], v[170:173], v[218:221], v[108:111]
	v_mfma_f32_16x16x32_bf16 v[100:103], v[178:181], v[218:221], v[100:103]
	v_mfma_f32_16x16x32_bf16 v[92:95], v[170:173], v[226:229], v[92:95]
	v_mfma_f32_16x16x32_bf16 v[84:87], v[178:181], v[226:229], v[84:87]
	s_setprio 0
	s_setprio 1
	v_mfma_f32_16x16x32_bf16 v[104:107], v[182:185], v[198:201], v[104:107]
	v_mfma_f32_16x16x32_bf16 v[96:99], v[190:193], v[198:201], v[96:99]
	v_mfma_f32_16x16x32_bf16 v[88:91], v[182:185], v[206:209], v[88:91]
	v_mfma_f32_16x16x32_bf16 v[80:83], v[190:193], v[206:209], v[80:83]
	v_mfma_f32_16x16x32_bf16 v[76:79], v[182:185], v[214:217], v[76:79]
	v_mfma_f32_16x16x32_bf16 v[72:75], v[190:193], v[214:217], v[72:75]
	v_mfma_f32_16x16x32_bf16 v[68:71], v[182:185], v[222:225], v[68:71]
	v_mfma_f32_16x16x32_bf16 v[64:67], v[190:193], v[222:225], v[64:67]
	v_mfma_f32_16x16x32_bf16 v[104:107], v[186:189], v[202:205], v[104:107]
	v_mfma_f32_16x16x32_bf16 v[96:99], v[194:197], v[202:205], v[96:99]
	v_mfma_f32_16x16x32_bf16 v[88:91], v[186:189], v[210:213], v[88:91]
	v_mfma_f32_16x16x32_bf16 v[80:83], v[194:197], v[210:213], v[80:83]
	v_mfma_f32_16x16x32_bf16 v[76:79], v[186:189], v[218:221], v[76:79]
	v_mfma_f32_16x16x32_bf16 v[72:75], v[194:197], v[218:221], v[72:75]
	v_mfma_f32_16x16x32_bf16 v[68:71], v[186:189], v[226:229], v[68:71]
	v_mfma_f32_16x16x32_bf16 v[64:67], v[194:197], v[226:229], v[64:67]
	s_setprio 0
	s_barrier
	s_add_i32 s63, s50, s1
	v_lshl_add_u64 v[232:233], s[44:45], 0, v[146:147]
	s_mov_b32 m0, s63
	ds_read_b128 v[198:201], v164 offset:16384
	ds_read_b128 v[202:205], v164 offset:17408
	ds_read_b128 v[206:209], v164 offset:18432
	ds_read_b128 v[210:213], v164 offset:19456
	ds_read_b128 v[214:217], v164 offset:20480
	ds_read_b128 v[218:221], v164 offset:21504
	ds_read_b128 v[222:225], v164 offset:22528
	ds_read_b128 v[226:229], v164 offset:23552
	global_load_lds_dwordx4 v[232:233], off
	s_add_i32 m0, s63, 0x2000
	s_add_u32 s64, s44, 0x80000
	v_lshl_add_u64 v[234:235], s[44:45], 0, v[148:149]
	s_addc_u32 s65, s45, 0
	s_add_i32 s63, s51, s1
	global_load_lds_dwordx4 v[234:235], off
	v_lshl_add_u64 v[236:237], s[64:65], 0, v[146:147]
	s_mov_b32 m0, s63
	v_mov_b32_e32 v231, v151
	global_load_lds_dwordx4 v[236:237], off
	v_lshl_add_u64 v[236:237], s[64:65], 0, v[148:149]
	s_add_i32 m0, s63, 0x2000
	s_nop 0
	global_load_lds_dwordx4 v[236:237], off
	s_mov_b32 m0, s4
	v_lshl_add_u64 v[236:237], s[46:47], 0, v[150:151]
	global_load_lds_dwordx4 v150, s[46:47]
	s_mov_b32 m0, s5
	s_nop 0
	global_load_lds_dwordx4 v230, s[46:47]
	s_waitcnt vmcnt(8)
	s_waitcnt lgkmcnt(0)
	v_lshl_add_u64 v[230:231], s[46:47], 0, v[230:231]
	s_barrier
	s_setprio 1
	v_mfma_f32_16x16x32_bf16 v[60:63], v[140:143], v[198:201], v[60:63]
	v_mfma_f32_16x16x32_bf16 v[56:59], v[174:177], v[198:201], v[56:59]
	v_mfma_f32_16x16x32_bf16 v[44:47], v[140:143], v[206:209], v[44:47]
	v_mfma_f32_16x16x32_bf16 v[36:39], v[174:177], v[206:209], v[36:39]
	v_mfma_f32_16x16x32_bf16 v[20:23], v[140:143], v[214:217], v[20:23]
	v_mfma_f32_16x16x32_bf16 v[12:15], v[174:177], v[214:217], v[12:15]
	v_mfma_f32_16x16x32_bf16 v[4:7], v[140:143], v[222:225], v[4:7]
	v_mfma_f32_16x16x32_bf16 v[0:3], v[174:177], v[222:225], v[0:3]
	v_mfma_f32_16x16x32_bf16 v[60:63], v[170:173], v[202:205], v[60:63]
	v_mfma_f32_16x16x32_bf16 v[56:59], v[178:181], v[202:205], v[56:59]
	v_mfma_f32_16x16x32_bf16 v[44:47], v[170:173], v[210:213], v[44:47]
	v_mfma_f32_16x16x32_bf16 v[36:39], v[178:181], v[210:213], v[36:39]
	v_mfma_f32_16x16x32_bf16 v[20:23], v[170:173], v[218:221], v[20:23]
	v_mfma_f32_16x16x32_bf16 v[12:15], v[178:181], v[218:221], v[12:15]
	v_mfma_f32_16x16x32_bf16 v[4:7], v[170:173], v[226:229], v[4:7]
	v_mfma_f32_16x16x32_bf16 v[0:3], v[178:181], v[226:229], v[0:3]
	s_setprio 0
	s_setprio 1
	v_mfma_f32_16x16x32_bf16 v[40:43], v[182:185], v[198:201], v[40:43]
	v_mfma_f32_16x16x32_bf16 v[32:35], v[190:193], v[198:201], v[32:35]
	v_mfma_f32_16x16x32_bf16 v[16:19], v[182:185], v[206:209], v[16:19]
	v_mfma_f32_16x16x32_bf16 v[8:11], v[190:193], v[206:209], v[8:11]
	v_mfma_f32_16x16x32_bf16 v[48:51], v[182:185], v[214:217], v[48:51]
	v_mfma_f32_16x16x32_bf16 v[52:55], v[190:193], v[214:217], v[52:55]
	v_mfma_f32_16x16x32_bf16 v[24:27], v[182:185], v[222:225], v[24:27]
	v_mfma_f32_16x16x32_bf16 v[28:31], v[190:193], v[222:225], v[28:31]
	v_mfma_f32_16x16x32_bf16 v[40:43], v[186:189], v[202:205], v[40:43]
	v_mfma_f32_16x16x32_bf16 v[32:35], v[194:197], v[202:205], v[32:35]
	v_mfma_f32_16x16x32_bf16 v[16:19], v[186:189], v[210:213], v[16:19]
	v_mfma_f32_16x16x32_bf16 v[8:11], v[194:197], v[210:213], v[8:11]
	v_mfma_f32_16x16x32_bf16 v[48:51], v[186:189], v[218:221], v[48:51]
	v_mfma_f32_16x16x32_bf16 v[52:55], v[194:197], v[218:221], v[52:55]
	v_mfma_f32_16x16x32_bf16 v[24:27], v[186:189], v[226:229], v[24:27]
	v_mfma_f32_16x16x32_bf16 v[28:31], v[194:197], v[226:229], v[28:31]
	s_setprio 0
	s_barrier
	s_add_i32 s63, 0, 0x18000
	v_add_u32_e32 v133, s63, v160
	s_add_i32 s64, 0, 0x1c000
	ds_read_b128 v[140:143], v133
	ds_read_b128 v[170:173], v133 offset:1024
	ds_read_b128 v[174:177], v133 offset:2048
	ds_read_b128 v[178:181], v133 offset:3072
	v_add_u32_e32 v133, s64, v160
	ds_read_b128 v[182:185], v133
	ds_read_b128 v[186:189], v133 offset:1024
	ds_read_b128 v[190:193], v133 offset:2048
	ds_read_b128 v[194:197], v133 offset:3072
	s_mov_b32 m0, s6
	ds_read_b128 v[198:201], v164 offset:32768
	ds_read_b128 v[202:205], v164 offset:33792
	ds_read_b128 v[206:209], v164 offset:34816
	ds_read_b128 v[210:213], v164 offset:35840
	ds_read_b128 v[214:217], v164 offset:36864
	ds_read_b128 v[218:221], v164 offset:37888
	ds_read_b128 v[222:225], v164 offset:38912
	ds_read_b128 v[226:229], v164 offset:39936
	global_load_lds_dwordx4 v129, s[46:47]
	s_mov_b32 m0, s7
	s_nop 0
	global_load_lds_dwordx4 v131, s[46:47]
	s_waitcnt vmcnt(8)
	s_waitcnt lgkmcnt(0)
	s_barrier
	s_setprio 1
	v_mfma_f32_16x16x32_bf16 v[124:127], v[140:143], v[198:201], v[124:127]
	v_mfma_f32_16x16x32_bf16 v[120:123], v[174:177], v[198:201], v[120:123]
	v_mfma_f32_16x16x32_bf16 v[116:119], v[140:143], v[206:209], v[116:119]
	v_mfma_f32_16x16x32_bf16 v[112:115], v[174:177], v[206:209], v[112:115]
	v_mfma_f32_16x16x32_bf16 v[108:111], v[140:143], v[214:217], v[108:111]
	v_mfma_f32_16x16x32_bf16 v[100:103], v[174:177], v[214:217], v[100:103]
	v_mfma_f32_16x16x32_bf16 v[92:95], v[140:143], v[222:225], v[92:95]
	v_mfma_f32_16x16x32_bf16 v[84:87], v[174:177], v[222:225], v[84:87]
	v_mfma_f32_16x16x32_bf16 v[124:127], v[170:173], v[202:205], v[124:127]
	v_mfma_f32_16x16x32_bf16 v[120:123], v[178:181], v[202:205], v[120:123]
	v_mfma_f32_16x16x32_bf16 v[116:119], v[170:173], v[210:213], v[116:119]
	v_mfma_f32_16x16x32_bf16 v[112:115], v[178:181], v[210:213], v[112:115]
	v_mfma_f32_16x16x32_bf16 v[108:111], v[170:173], v[218:221], v[108:111]
	v_mfma_f32_16x16x32_bf16 v[100:103], v[178:181], v[218:221], v[100:103]
	v_mfma_f32_16x16x32_bf16 v[92:95], v[170:173], v[226:229], v[92:95]
	v_mfma_f32_16x16x32_bf16 v[84:87], v[178:181], v[226:229], v[84:87]
	s_setprio 0
	s_setprio 1
	v_mfma_f32_16x16x32_bf16 v[104:107], v[182:185], v[198:201], v[104:107]
	v_mfma_f32_16x16x32_bf16 v[96:99], v[190:193], v[198:201], v[96:99]
	v_mfma_f32_16x16x32_bf16 v[88:91], v[182:185], v[206:209], v[88:91]
	v_mfma_f32_16x16x32_bf16 v[80:83], v[190:193], v[206:209], v[80:83]
	v_mfma_f32_16x16x32_bf16 v[76:79], v[182:185], v[214:217], v[76:79]
	v_mfma_f32_16x16x32_bf16 v[72:75], v[190:193], v[214:217], v[72:75]
	v_mfma_f32_16x16x32_bf16 v[68:71], v[182:185], v[222:225], v[68:71]
	v_mfma_f32_16x16x32_bf16 v[64:67], v[190:193], v[222:225], v[64:67]
	v_mfma_f32_16x16x32_bf16 v[104:107], v[186:189], v[202:205], v[104:107]
	v_mfma_f32_16x16x32_bf16 v[96:99], v[194:197], v[202:205], v[96:99]
	v_mfma_f32_16x16x32_bf16 v[88:91], v[186:189], v[210:213], v[88:91]
	v_mfma_f32_16x16x32_bf16 v[80:83], v[194:197], v[210:213], v[80:83]
	v_mfma_f32_16x16x32_bf16 v[76:79], v[186:189], v[218:221], v[76:79]
	v_mfma_f32_16x16x32_bf16 v[72:75], v[194:197], v[218:221], v[72:75]
	v_mfma_f32_16x16x32_bf16 v[68:71], v[186:189], v[226:229], v[68:71]
	v_mfma_f32_16x16x32_bf16 v[64:67], v[194:197], v[226:229], v[64:67]
	s_setprio 0
	s_barrier
	s_add_i32 s46, s63, s1
	v_lshl_add_u64 v[232:233], v[232:233], 0, s[24:25]
	s_mov_b32 m0, s46
	ds_read_b128 v[198:201], v164 offset:49152
	ds_read_b128 v[202:205], v164 offset:50176
	ds_read_b128 v[206:209], v164 offset:51200
	ds_read_b128 v[210:213], v164 offset:52224
	ds_read_b128 v[214:217], v164 offset:53248
	ds_read_b128 v[218:221], v164 offset:54272
	ds_read_b128 v[222:225], v164 offset:55296
	ds_read_b128 v[226:229], v164 offset:56320
	global_load_lds_dwordx4 v[232:233], off
	s_add_i32 m0, s46, 0x2000
	s_add_u32 s44, s44, 0x80080
	v_lshl_add_u64 v[232:233], v[234:235], 0, s[24:25]
	s_addc_u32 s45, s45, 0
	s_add_i32 s46, s64, s1
	global_load_lds_dwordx4 v[232:233], off
	v_lshl_add_u64 v[232:233], s[44:45], 0, v[146:147]
	s_mov_b32 m0, s46
	v_lshl_add_u64 v[230:231], v[230:231], 0, s[24:25]
	global_load_lds_dwordx4 v[232:233], off
	v_lshl_add_u64 v[232:233], s[44:45], 0, v[148:149]
	s_add_i32 m0, s46, 0x2000
	s_nop 0
	global_load_lds_dwordx4 v[232:233], off
	v_lshl_add_u64 v[232:233], v[236:237], 0, s[24:25]
	s_mov_b32 m0, s9
	s_nop 0
	global_load_lds_dwordx4 v[232:233], off
	s_mov_b32 m0, s48
	s_nop 0
	global_load_lds_dwordx4 v[230:231], off
	s_waitcnt vmcnt(8)
	s_waitcnt lgkmcnt(0)
	s_barrier
	s_setprio 1
	v_mfma_f32_16x16x32_bf16 v[60:63], v[140:143], v[198:201], v[60:63]
	v_mfma_f32_16x16x32_bf16 v[56:59], v[174:177], v[198:201], v[56:59]
	v_mfma_f32_16x16x32_bf16 v[44:47], v[140:143], v[206:209], v[44:47]
	v_mfma_f32_16x16x32_bf16 v[36:39], v[174:177], v[206:209], v[36:39]
	v_mfma_f32_16x16x32_bf16 v[20:23], v[140:143], v[214:217], v[20:23]
	v_mfma_f32_16x16x32_bf16 v[12:15], v[174:177], v[214:217], v[12:15]
	v_mfma_f32_16x16x32_bf16 v[4:7], v[140:143], v[222:225], v[4:7]
	v_mfma_f32_16x16x32_bf16 v[0:3], v[174:177], v[222:225], v[0:3]
	v_mfma_f32_16x16x32_bf16 v[60:63], v[170:173], v[202:205], v[60:63]
	v_mfma_f32_16x16x32_bf16 v[56:59], v[178:181], v[202:205], v[56:59]
	v_mfma_f32_16x16x32_bf16 v[44:47], v[170:173], v[210:213], v[44:47]
	v_mfma_f32_16x16x32_bf16 v[36:39], v[178:181], v[210:213], v[36:39]
	v_mfma_f32_16x16x32_bf16 v[20:23], v[170:173], v[218:221], v[20:23]
	v_mfma_f32_16x16x32_bf16 v[12:15], v[178:181], v[218:221], v[12:15]
	v_mfma_f32_16x16x32_bf16 v[4:7], v[170:173], v[226:229], v[4:7]
	v_mfma_f32_16x16x32_bf16 v[0:3], v[178:181], v[226:229], v[0:3]
	s_setprio 0
	s_setprio 1
	v_mfma_f32_16x16x32_bf16 v[40:43], v[182:185], v[198:201], v[40:43]
	v_mfma_f32_16x16x32_bf16 v[32:35], v[190:193], v[198:201], v[32:35]
	v_mfma_f32_16x16x32_bf16 v[16:19], v[182:185], v[206:209], v[16:19]
	v_mfma_f32_16x16x32_bf16 v[8:11], v[190:193], v[206:209], v[8:11]
	v_mfma_f32_16x16x32_bf16 v[48:51], v[182:185], v[214:217], v[48:51]
	v_mfma_f32_16x16x32_bf16 v[52:55], v[190:193], v[214:217], v[52:55]
	v_mfma_f32_16x16x32_bf16 v[24:27], v[182:185], v[222:225], v[24:27]
	v_mfma_f32_16x16x32_bf16 v[28:31], v[190:193], v[222:225], v[28:31]
	v_mfma_f32_16x16x32_bf16 v[40:43], v[186:189], v[202:205], v[40:43]
	v_mfma_f32_16x16x32_bf16 v[32:35], v[194:197], v[202:205], v[32:35]
	v_mfma_f32_16x16x32_bf16 v[16:19], v[186:189], v[210:213], v[16:19]
	v_mfma_f32_16x16x32_bf16 v[8:11], v[194:197], v[210:213], v[8:11]
	v_mfma_f32_16x16x32_bf16 v[48:51], v[186:189], v[218:221], v[48:51]
	v_mfma_f32_16x16x32_bf16 v[52:55], v[194:197], v[218:221], v[52:55]
	v_mfma_f32_16x16x32_bf16 v[24:27], v[186:189], v[226:229], v[24:27]
	v_mfma_f32_16x16x32_bf16 v[28:31], v[194:197], v[226:229], v[28:31]
	s_setprio 0
	s_barrier
	s_add_i32 s62, s62, 2
	s_add_u32 s12, s12, 0x100
	s_addc_u32 s13, s13, 0
	s_cmp_gt_u32 s62, 29
	s_cbranch_scc0 .LBB0_964
	s_and_b64 vcc, exec, s[26:27]
	s_cbranch_vccz .LBB0_967
	s_barrier

.LBB0_1359:
	v_add_u32_e32 v165, s51, v143
	ds_read_b128 v[166:169], v165
	ds_read_b128 v[170:173], v165 offset:1024
	ds_read_b128 v[174:177], v165 offset:2048
	ds_read_b128 v[178:181], v165 offset:3072
	v_add_u32_e32 v165, s52, v143
	ds_read_b128 v[182:185], v165
	ds_read_b128 v[186:189], v165 offset:1024
	ds_read_b128 v[190:193], v165 offset:2048
	ds_read_b128 v[194:197], v165 offset:3072
	s_cmpk_eq_i32 s14, 0x1000
	s_cselect_b64 vcc, -1, 0
	s_and_b64 s[48:49], vcc, exec
	s_cselect_b32 s48, 0, s14
	v_lshl_add_u64 v[154:155], v[148:149], 0, s[14:15]
	s_cselect_b32 s49, 0, s15
	s_add_u32 s48, s22, s48
	v_cndmask_b32_e32 v132, v146, v160, vcc
	v_cndmask_b32_e32 v139, v140, v162, vcc
	v_cndmask_b32_e32 v230, v142, v161, vcc
	v_cndmask_b32_e32 v141, v138, v163, vcc
	v_cndmask_b32_e32 v154, v154, v164, vcc
	v_cndmask_b32_e32 v155, v155, v135, vcc
	s_addc_u32 s49, s23, s49
	v_lshl_add_u64 v[232:233], v[152:153], 0, s[14:15]
	s_mov_b32 m0, s53
	v_lshl_add_u64 v[232:233], v[232:233], 0, s[42:43]
	ds_read_b128 v[198:201], v159
	ds_read_b128 v[202:205], v159 offset:1024
	ds_read_b128 v[206:209], v159 offset:2048
	ds_read_b128 v[210:213], v159 offset:3072
	ds_read_b128 v[214:217], v159 offset:4096
	ds_read_b128 v[218:221], v159 offset:5120
	ds_read_b128 v[222:225], v159 offset:6144
	ds_read_b128 v[226:229], v159 offset:7168
	global_load_lds_dwordx4 v[232:233], off
	v_lshl_add_u64 v[232:233], v[150:151], 0, s[14:15]
	v_lshl_add_u64 v[232:233], v[232:233], 0, s[42:43]
	s_mov_b32 m0, s55
	s_nop 0
	global_load_lds_dwordx4 v[232:233], off
	s_waitcnt vmcnt(8)
	s_waitcnt lgkmcnt(0)
	s_barrier
	s_setprio 1
	v_mfma_f32_16x16x32_bf16 v[124:127], v[166:169], v[198:201], v[124:127]
	v_mfma_f32_16x16x32_bf16 v[120:123], v[174:177], v[198:201], v[120:123]
	v_mfma_f32_16x16x32_bf16 v[108:111], v[166:169], v[206:209], v[108:111]
	v_mfma_f32_16x16x32_bf16 v[104:107], v[174:177], v[206:209], v[104:107]
	v_mfma_f32_16x16x32_bf16 v[92:95], v[166:169], v[214:217], v[92:95]
	v_mfma_f32_16x16x32_bf16 v[88:91], v[174:177], v[214:217], v[88:91]
	v_mfma_f32_16x16x32_bf16 v[76:79], v[166:169], v[222:225], v[76:79]
	v_mfma_f32_16x16x32_bf16 v[72:75], v[174:177], v[222:225], v[72:75]
	v_mfma_f32_16x16x32_bf16 v[124:127], v[170:173], v[202:205], v[124:127]
	v_mfma_f32_16x16x32_bf16 v[120:123], v[178:181], v[202:205], v[120:123]
	v_mfma_f32_16x16x32_bf16 v[108:111], v[170:173], v[210:213], v[108:111]
	v_mfma_f32_16x16x32_bf16 v[104:107], v[178:181], v[210:213], v[104:107]
	v_mfma_f32_16x16x32_bf16 v[92:95], v[170:173], v[218:221], v[92:95]
	v_mfma_f32_16x16x32_bf16 v[88:91], v[178:181], v[218:221], v[88:91]
	v_mfma_f32_16x16x32_bf16 v[76:79], v[170:173], v[226:229], v[76:79]
	v_mfma_f32_16x16x32_bf16 v[72:75], v[178:181], v[226:229], v[72:75]
	s_setprio 0
	s_setprio 1
	v_mfma_f32_16x16x32_bf16 v[116:119], v[182:185], v[198:201], v[116:119]
	v_mfma_f32_16x16x32_bf16 v[112:115], v[190:193], v[198:201], v[112:115]
	v_mfma_f32_16x16x32_bf16 v[100:103], v[182:185], v[206:209], v[100:103]
	v_mfma_f32_16x16x32_bf16 v[96:99], v[190:193], v[206:209], v[96:99]
	v_mfma_f32_16x16x32_bf16 v[84:87], v[182:185], v[214:217], v[84:87]
	v_mfma_f32_16x16x32_bf16 v[80:83], v[190:193], v[214:217], v[80:83]
	v_mfma_f32_16x16x32_bf16 v[68:71], v[182:185], v[222:225], v[68:71]
	v_mfma_f32_16x16x32_bf16 v[64:67], v[190:193], v[222:225], v[64:67]
	v_mfma_f32_16x16x32_bf16 v[116:119], v[186:189], v[202:205], v[116:119]
	v_mfma_f32_16x16x32_bf16 v[112:115], v[194:197], v[202:205], v[112:115]
	v_mfma_f32_16x16x32_bf16 v[100:103], v[186:189], v[210:213], v[100:103]
	v_mfma_f32_16x16x32_bf16 v[96:99], v[194:197], v[210:213], v[96:99]
	v_mfma_f32_16x16x32_bf16 v[84:87], v[186:189], v[218:221], v[84:87]
	v_mfma_f32_16x16x32_bf16 v[80:83], v[194:197], v[218:221], v[80:83]
	v_mfma_f32_16x16x32_bf16 v[68:71], v[186:189], v[226:229], v[68:71]
	v_mfma_f32_16x16x32_bf16 v[64:67], v[194:197], v[226:229], v[64:67]
	s_setprio 0
	s_barrier
	s_mov_b32 m0, s57
	v_lshl_add_u64 v[232:233], v[154:155], 0, v[128:129]
	ds_read_b128 v[198:201], v159 offset:16384
	ds_read_b128 v[202:205], v159 offset:17408
	ds_read_b128 v[206:209], v159 offset:18432
	ds_read_b128 v[210:213], v159 offset:19456
	ds_read_b128 v[214:217], v159 offset:20480
	ds_read_b128 v[218:221], v159 offset:21504
	ds_read_b128 v[222:225], v159 offset:22528
	ds_read_b128 v[226:229], v159 offset:23552
	global_load_lds_dwordx4 v[232:233], off
	v_lshl_add_u64 v[234:235], v[154:155], 0, v[130:131]
	s_mov_b32 m0, s59
	v_lshl_add_u64 v[236:237], v[154:155], 0, s[30:31]
	global_load_lds_dwordx4 v[234:235], off
	v_lshl_add_u64 v[238:239], v[236:237], 0, v[128:129]
	s_mov_b32 m0, s60
	v_lshl_add_u64 v[236:237], v[236:237], 0, v[130:131]
	global_load_lds_dwordx4 v[238:239], off
	s_mov_b32 m0, s61
	v_mov_b32_e32 v231, v133
	global_load_lds_dwordx4 v[236:237], off
	s_mov_b32 m0, s1
	v_lshl_add_u64 v[236:237], s[48:49], 0, v[132:133]
	global_load_lds_dwordx4 v132, s[48:49]
	s_mov_b32 m0, s4
	s_nop 0
	global_load_lds_dwordx4 v230, s[48:49]
	s_waitcnt vmcnt(8)
	s_waitcnt lgkmcnt(0)
	v_lshl_add_u64 v[230:231], s[48:49], 0, v[230:231]
	s_barrier
	s_setprio 1
	v_mfma_f32_16x16x32_bf16 v[60:63], v[166:169], v[198:201], v[60:63]
	v_mfma_f32_16x16x32_bf16 v[56:59], v[174:177], v[198:201], v[56:59]
	v_mfma_f32_16x16x32_bf16 v[44:47], v[166:169], v[206:209], v[44:47]
	v_mfma_f32_16x16x32_bf16 v[36:39], v[174:177], v[206:209], v[36:39]
	v_mfma_f32_16x16x32_bf16 v[20:23], v[166:169], v[214:217], v[20:23]
	v_mfma_f32_16x16x32_bf16 v[8:11], v[174:177], v[214:217], v[8:11]
	v_mfma_f32_16x16x32_bf16 v[4:7], v[166:169], v[222:225], v[4:7]
	v_mfma_f32_16x16x32_bf16 v[0:3], v[174:177], v[222:225], v[0:3]
	v_mfma_f32_16x16x32_bf16 v[60:63], v[170:173], v[202:205], v[60:63]
	v_mfma_f32_16x16x32_bf16 v[56:59], v[178:181], v[202:205], v[56:59]
	v_mfma_f32_16x16x32_bf16 v[44:47], v[170:173], v[210:213], v[44:47]
	v_mfma_f32_16x16x32_bf16 v[36:39], v[178:181], v[210:213], v[36:39]
	v_mfma_f32_16x16x32_bf16 v[20:23], v[170:173], v[218:221], v[20:23]
	v_mfma_f32_16x16x32_bf16 v[8:11], v[178:181], v[218:221], v[8:11]
	v_mfma_f32_16x16x32_bf16 v[4:7], v[170:173], v[226:229], v[4:7]
	v_mfma_f32_16x16x32_bf16 v[0:3], v[178:181], v[226:229], v[0:3]
	s_setprio 0
	s_setprio 1
	v_mfma_f32_16x16x32_bf16 v[52:55], v[182:185], v[198:201], v[52:55]
	v_mfma_f32_16x16x32_bf16 v[48:51], v[190:193], v[198:201], v[48:51]
	v_mfma_f32_16x16x32_bf16 v[28:31], v[182:185], v[206:209], v[28:31]
	v_mfma_f32_16x16x32_bf16 v[24:27], v[190:193], v[206:209], v[24:27]
	v_mfma_f32_16x16x32_bf16 v[40:43], v[182:185], v[214:217], v[40:43]
	v_mfma_f32_16x16x32_bf16 v[32:35], v[190:193], v[214:217], v[32:35]
	v_mfma_f32_16x16x32_bf16 v[16:19], v[182:185], v[222:225], v[16:19]
	v_mfma_f32_16x16x32_bf16 v[12:15], v[190:193], v[222:225], v[12:15]
	v_mfma_f32_16x16x32_bf16 v[52:55], v[186:189], v[202:205], v[52:55]
	v_mfma_f32_16x16x32_bf16 v[48:51], v[194:197], v[202:205], v[48:51]
	v_mfma_f32_16x16x32_bf16 v[28:31], v[186:189], v[210:213], v[28:31]
	v_mfma_f32_16x16x32_bf16 v[24:27], v[194:197], v[210:213], v[24:27]
	v_mfma_f32_16x16x32_bf16 v[40:43], v[186:189], v[218:221], v[40:43]
	v_mfma_f32_16x16x32_bf16 v[32:35], v[194:197], v[218:221], v[32:35]
	v_mfma_f32_16x16x32_bf16 v[16:19], v[186:189], v[226:229], v[16:19]
	v_mfma_f32_16x16x32_bf16 v[12:15], v[194:197], v[226:229], v[12:15]
	s_setprio 0
	s_barrier
	v_add_u32_e32 v132, s62, v143
	ds_read_b128 v[166:169], v132
	ds_read_b128 v[170:173], v132 offset:1024
	ds_read_b128 v[174:177], v132 offset:2048
	ds_read_b128 v[178:181], v132 offset:3072
	v_add_u32_e32 v132, s63, v143
	ds_read_b128 v[182:185], v132
	ds_read_b128 v[186:189], v132 offset:1024
	ds_read_b128 v[190:193], v132 offset:2048
	ds_read_b128 v[194:197], v132 offset:3072
	s_mov_b32 m0, s5
	ds_read_b128 v[198:201], v159 offset:32768
	ds_read_b128 v[202:205], v159 offset:33792
	ds_read_b128 v[206:209], v159 offset:34816
	ds_read_b128 v[210:213], v159 offset:35840
	ds_read_b128 v[214:217], v159 offset:36864
	ds_read_b128 v[218:221], v159 offset:37888
	ds_read_b128 v[222:225], v159 offset:38912
	ds_read_b128 v[226:229], v159 offset:39936
	global_load_lds_dwordx4 v139, s[48:49]
	s_mov_b32 m0, s6
	s_nop 0
	global_load_lds_dwordx4 v141, s[48:49]
	s_waitcnt vmcnt(8)
	s_waitcnt lgkmcnt(0)
	s_barrier
	s_setprio 1
	v_mfma_f32_16x16x32_bf16 v[124:127], v[166:169], v[198:201], v[124:127]
	v_mfma_f32_16x16x32_bf16 v[120:123], v[174:177], v[198:201], v[120:123]
	v_mfma_f32_16x16x32_bf16 v[108:111], v[166:169], v[206:209], v[108:111]
	v_mfma_f32_16x16x32_bf16 v[104:107], v[174:177], v[206:209], v[104:107]
	v_mfma_f32_16x16x32_bf16 v[92:95], v[166:169], v[214:217], v[92:95]
	v_mfma_f32_16x16x32_bf16 v[88:91], v[174:177], v[214:217], v[88:91]
	v_mfma_f32_16x16x32_bf16 v[76:79], v[166:169], v[222:225], v[76:79]
	v_mfma_f32_16x16x32_bf16 v[72:75], v[174:177], v[222:225], v[72:75]
	v_mfma_f32_16x16x32_bf16 v[124:127], v[170:173], v[202:205], v[124:127]
	v_mfma_f32_16x16x32_bf16 v[120:123], v[178:181], v[202:205], v[120:123]
	v_mfma_f32_16x16x32_bf16 v[108:111], v[170:173], v[210:213], v[108:111]
	v_mfma_f32_16x16x32_bf16 v[104:107], v[178:181], v[210:213], v[104:107]
	v_mfma_f32_16x16x32_bf16 v[92:95], v[170:173], v[218:221], v[92:95]
	v_mfma_f32_16x16x32_bf16 v[88:91], v[178:181], v[218:221], v[88:91]
	v_mfma_f32_16x16x32_bf16 v[76:79], v[170:173], v[226:229], v[76:79]
	v_mfma_f32_16x16x32_bf16 v[72:75], v[178:181], v[226:229], v[72:75]
	s_setprio 0
	s_setprio 1
	v_mfma_f32_16x16x32_bf16 v[116:119], v[182:185], v[198:201], v[116:119]
	v_mfma_f32_16x16x32_bf16 v[112:115], v[190:193], v[198:201], v[112:115]
	v_mfma_f32_16x16x32_bf16 v[100:103], v[182:185], v[206:209], v[100:103]
	v_mfma_f32_16x16x32_bf16 v[96:99], v[190:193], v[206:209], v[96:99]
	v_mfma_f32_16x16x32_bf16 v[84:87], v[182:185], v[214:217], v[84:87]
	v_mfma_f32_16x16x32_bf16 v[80:83], v[190:193], v[214:217], v[80:83]
	v_mfma_f32_16x16x32_bf16 v[68:71], v[182:185], v[222:225], v[68:71]
	v_mfma_f32_16x16x32_bf16 v[64:67], v[190:193], v[222:225], v[64:67]
	v_mfma_f32_16x16x32_bf16 v[116:119], v[186:189], v[202:205], v[116:119]
	v_mfma_f32_16x16x32_bf16 v[112:115], v[194:197], v[202:205], v[112:115]
	v_mfma_f32_16x16x32_bf16 v[100:103], v[186:189], v[210:213], v[100:103]
	v_mfma_f32_16x16x32_bf16 v[96:99], v[194:197], v[210:213], v[96:99]
	v_mfma_f32_16x16x32_bf16 v[84:87], v[186:189], v[218:221], v[84:87]
	v_mfma_f32_16x16x32_bf16 v[80:83], v[194:197], v[218:221], v[80:83]
	v_mfma_f32_16x16x32_bf16 v[68:71], v[186:189], v[226:229], v[68:71]
	v_mfma_f32_16x16x32_bf16 v[64:67], v[194:197], v[226:229], v[64:67]
	s_setprio 0
	s_barrier
	s_add_i32 s48, s62, s0
	v_lshl_add_u64 v[232:233], v[232:233], 0, s[36:37]
	s_mov_b32 m0, s48
	ds_read_b128 v[198:201], v159 offset:49152
	ds_read_b128 v[202:205], v159 offset:50176
	ds_read_b128 v[206:209], v159 offset:51200
	ds_read_b128 v[210:213], v159 offset:52224
	ds_read_b128 v[214:217], v159 offset:53248
	ds_read_b128 v[218:221], v159 offset:54272
	ds_read_b128 v[222:225], v159 offset:55296
	ds_read_b128 v[226:229], v159 offset:56320
	global_load_lds_dwordx4 v[232:233], off
	v_lshl_add_u64 v[232:233], v[234:235], 0, s[36:37]
	s_add_i32 m0, s48, 0x2000
	v_lshl_add_u64 v[154:155], v[154:155], 0, s[38:39]
	s_add_i32 s48, s63, s0
	global_load_lds_dwordx4 v[232:233], off
	v_lshl_add_u64 v[232:233], v[154:155], 0, v[128:129]
	s_mov_b32 m0, s48
	v_lshl_add_u64 v[154:155], v[154:155], 0, v[130:131]
	global_load_lds_dwordx4 v[232:233], off
	s_add_i32 m0, s48, 0x2000
	s_nop 0
	global_load_lds_dwordx4 v[154:155], off
	v_lshl_add_u64 v[154:155], v[236:237], 0, s[36:37]
	s_mov_b32 m0, s9
	s_nop 0
	global_load_lds_dwordx4 v[154:155], off
	v_lshl_add_u64 v[154:155], v[230:231], 0, s[36:37]
	s_mov_b32 m0, s28
	s_nop 0
	global_load_lds_dwordx4 v[154:155], off
	s_waitcnt vmcnt(8)
	s_waitcnt lgkmcnt(0)
	s_barrier
	s_setprio 1
	v_mfma_f32_16x16x32_bf16 v[60:63], v[166:169], v[198:201], v[60:63]
	v_mfma_f32_16x16x32_bf16 v[56:59], v[174:177], v[198:201], v[56:59]
	v_mfma_f32_16x16x32_bf16 v[44:47], v[166:169], v[206:209], v[44:47]
	v_mfma_f32_16x16x32_bf16 v[36:39], v[174:177], v[206:209], v[36:39]
	v_mfma_f32_16x16x32_bf16 v[20:23], v[166:169], v[214:217], v[20:23]
	v_mfma_f32_16x16x32_bf16 v[8:11], v[174:177], v[214:217], v[8:11]
	v_mfma_f32_16x16x32_bf16 v[4:7], v[166:169], v[222:225], v[4:7]
	v_mfma_f32_16x16x32_bf16 v[0:3], v[174:177], v[222:225], v[0:3]
	v_mfma_f32_16x16x32_bf16 v[60:63], v[170:173], v[202:205], v[60:63]
	v_mfma_f32_16x16x32_bf16 v[56:59], v[178:181], v[202:205], v[56:59]
	v_mfma_f32_16x16x32_bf16 v[44:47], v[170:173], v[210:213], v[44:47]
	v_mfma_f32_16x16x32_bf16 v[36:39], v[178:181], v[210:213], v[36:39]
	v_mfma_f32_16x16x32_bf16 v[20:23], v[170:173], v[218:221], v[20:23]
	v_mfma_f32_16x16x32_bf16 v[8:11], v[178:181], v[218:221], v[8:11]
	v_mfma_f32_16x16x32_bf16 v[4:7], v[170:173], v[226:229], v[4:7]
	v_mfma_f32_16x16x32_bf16 v[0:3], v[178:181], v[226:229], v[0:3]
	s_setprio 0
	s_setprio 1
	v_mfma_f32_16x16x32_bf16 v[52:55], v[182:185], v[198:201], v[52:55]
	v_mfma_f32_16x16x32_bf16 v[48:51], v[190:193], v[198:201], v[48:51]
	v_mfma_f32_16x16x32_bf16 v[28:31], v[182:185], v[206:209], v[28:31]
	v_mfma_f32_16x16x32_bf16 v[24:27], v[190:193], v[206:209], v[24:27]
	v_mfma_f32_16x16x32_bf16 v[40:43], v[182:185], v[214:217], v[40:43]
	v_mfma_f32_16x16x32_bf16 v[32:35], v[190:193], v[214:217], v[32:35]
	v_mfma_f32_16x16x32_bf16 v[16:19], v[182:185], v[222:225], v[16:19]
	v_mfma_f32_16x16x32_bf16 v[12:15], v[190:193], v[222:225], v[12:15]
	v_mfma_f32_16x16x32_bf16 v[52:55], v[186:189], v[202:205], v[52:55]
	v_mfma_f32_16x16x32_bf16 v[48:51], v[194:197], v[202:205], v[48:51]
	v_mfma_f32_16x16x32_bf16 v[28:31], v[186:189], v[210:213], v[28:31]
	v_mfma_f32_16x16x32_bf16 v[24:27], v[194:197], v[210:213], v[24:27]
	v_mfma_f32_16x16x32_bf16 v[40:43], v[186:189], v[218:221], v[40:43]
	v_mfma_f32_16x16x32_bf16 v[32:35], v[194:197], v[218:221], v[32:35]
	v_mfma_f32_16x16x32_bf16 v[16:19], v[186:189], v[226:229], v[16:19]
	v_mfma_f32_16x16x32_bf16 v[12:15], v[194:197], v[226:229], v[12:15]
	s_setprio 0
	s_barrier
	s_add_i32 s47, s47, 2
	s_add_u32 s14, s14, 0x100
	s_addc_u32 s15, s15, 0
	s_cmp_gt_u32 s47, 29
	s_cbranch_scc0 .LBB0_1359
	s_and_b64 vcc, exec, s[40:41]
	s_cbranch_vccz .LBB0_1362
	s_barrier

.LBB0_1571:
	ds_read_b128 v[170:173], v163
	ds_read_b128 v[174:177], v163 offset:1024
	ds_read_b128 v[178:181], v163 offset:2048
	ds_read_b128 v[182:185], v163 offset:3072
	ds_read_b128 v[186:189], v164
	ds_read_b128 v[190:193], v164 offset:1024
	ds_read_b128 v[194:197], v164 offset:2048
	ds_read_b128 v[198:201], v164 offset:3072
	s_add_u32 s46, s42, s10
	s_addc_u32 s47, s43, s11
	s_cmpk_eq_i32 s10, 0x1000
	s_cselect_b64 vcc, -1, 0
	s_and_b64 s[44:45], vcc, exec
	s_cselect_b32 s64, 0, s10
	s_cselect_b32 s63, 0, s11
	s_cselect_b32 s44, s39, s46
	s_cselect_b32 s45, s13, s47
	s_add_u32 s46, s20, s64
	v_cndmask_b32_e32 v140, v128, v166, vcc
	v_cndmask_b32_e32 v129, v132, v168, vcc
	v_cndmask_b32_e32 v154, v130, v167, vcc
	v_cndmask_b32_e32 v131, v134, v169, vcc
	s_addc_u32 s47, s21, s63
	v_lshl_add_u64 v[234:235], v[152:153], 0, s[10:11]
	v_lshl_add_u64 v[234:235], v[234:235], 0, s[18:19]
	s_add_i32 m0, s5, 0xc000
	ds_read_b128 v[202:205], v165
	ds_read_b128 v[206:209], v165 offset:1024
	ds_read_b128 v[210:213], v165 offset:2048
	ds_read_b128 v[214:217], v165 offset:3072
	ds_read_b128 v[218:221], v165 offset:4096
	ds_read_b128 v[222:225], v165 offset:5120
	ds_read_b128 v[226:229], v165 offset:6144
	ds_read_b128 v[230:233], v165 offset:7168
	global_load_lds_dwordx4 v[234:235], off
	v_lshl_add_u64 v[234:235], v[150:151], 0, s[10:11]
	v_lshl_add_u64 v[234:235], v[234:235], 0, s[18:19]
	s_add_i32 m0, s5, 0xe000
	s_nop 0
	global_load_lds_dwordx4 v[234:235], off
	s_waitcnt vmcnt(8)
	s_waitcnt lgkmcnt(0)
	s_barrier
	s_setprio 1
	v_mfma_f32_16x16x32_bf16 v[60:63], v[170:173], v[202:205], v[60:63]
	v_mfma_f32_16x16x32_bf16 v[56:59], v[178:181], v[202:205], v[56:59]
	v_mfma_f32_16x16x32_bf16 v[52:55], v[170:173], v[210:213], v[52:55]
	v_mfma_f32_16x16x32_bf16 v[48:51], v[178:181], v[210:213], v[48:51]
	v_mfma_f32_16x16x32_bf16 v[44:47], v[170:173], v[218:221], v[44:47]
	v_mfma_f32_16x16x32_bf16 v[40:43], v[178:181], v[218:221], v[40:43]
	v_mfma_f32_16x16x32_bf16 v[36:39], v[170:173], v[226:229], v[36:39]
	v_mfma_f32_16x16x32_bf16 v[32:35], v[178:181], v[226:229], v[32:35]
	v_mfma_f32_16x16x32_bf16 v[60:63], v[174:177], v[206:209], v[60:63]
	v_mfma_f32_16x16x32_bf16 v[56:59], v[182:185], v[206:209], v[56:59]
	v_mfma_f32_16x16x32_bf16 v[52:55], v[174:177], v[214:217], v[52:55]
	v_mfma_f32_16x16x32_bf16 v[48:51], v[182:185], v[214:217], v[48:51]
	v_mfma_f32_16x16x32_bf16 v[44:47], v[174:177], v[222:225], v[44:47]
	v_mfma_f32_16x16x32_bf16 v[40:43], v[182:185], v[222:225], v[40:43]
	v_mfma_f32_16x16x32_bf16 v[36:39], v[174:177], v[230:233], v[36:39]
	v_mfma_f32_16x16x32_bf16 v[32:35], v[182:185], v[230:233], v[32:35]
	s_setprio 0
	s_setprio 1
	v_mfma_f32_16x16x32_bf16 v[124:127], v[186:189], v[202:205], v[124:127]
	v_mfma_f32_16x16x32_bf16 v[120:123], v[194:197], v[202:205], v[120:123]
	v_mfma_f32_16x16x32_bf16 v[116:119], v[186:189], v[210:213], v[116:119]
	v_mfma_f32_16x16x32_bf16 v[112:115], v[194:197], v[210:213], v[112:115]
	v_mfma_f32_16x16x32_bf16 v[108:111], v[186:189], v[218:221], v[108:111]
	v_mfma_f32_16x16x32_bf16 v[104:107], v[194:197], v[218:221], v[104:107]
	v_mfma_f32_16x16x32_bf16 v[100:103], v[186:189], v[226:229], v[100:103]
	v_mfma_f32_16x16x32_bf16 v[96:99], v[194:197], v[226:229], v[96:99]
	v_mfma_f32_16x16x32_bf16 v[124:127], v[190:193], v[206:209], v[124:127]
	v_mfma_f32_16x16x32_bf16 v[120:123], v[198:201], v[206:209], v[120:123]
	v_mfma_f32_16x16x32_bf16 v[116:119], v[190:193], v[214:217], v[116:119]
	v_mfma_f32_16x16x32_bf16 v[112:115], v[198:201], v[214:217], v[112:115]
	v_mfma_f32_16x16x32_bf16 v[108:111], v[190:193], v[222:225], v[108:111]
	v_mfma_f32_16x16x32_bf16 v[104:107], v[198:201], v[222:225], v[104:107]
	v_mfma_f32_16x16x32_bf16 v[100:103], v[190:193], v[230:233], v[100:103]
	v_mfma_f32_16x16x32_bf16 v[96:99], v[198:201], v[230:233], v[96:99]
	s_setprio 0
	s_barrier
	s_add_i32 s63, s55, s0
	v_lshl_add_u64 v[234:235], s[44:45], 0, v[136:137]
	s_mov_b32 m0, s63
	ds_read_b128 v[202:205], v165 offset:16384
	ds_read_b128 v[206:209], v165 offset:17408
	ds_read_b128 v[210:213], v165 offset:18432
	ds_read_b128 v[214:217], v165 offset:19456
	ds_read_b128 v[218:221], v165 offset:20480
	ds_read_b128 v[222:225], v165 offset:21504
	ds_read_b128 v[226:229], v165 offset:22528
	ds_read_b128 v[230:233], v165 offset:23552
	global_load_lds_dwordx4 v[234:235], off
	s_add_i32 m0, s63, 0x2000
	s_add_u32 s64, s44, 0x80000
	v_lshl_add_u64 v[236:237], s[44:45], 0, v[138:139]
	s_addc_u32 s65, s45, 0
	s_add_i32 s63, s57, s0
	global_load_lds_dwordx4 v[236:237], off
	v_lshl_add_u64 v[238:239], s[64:65], 0, v[136:137]
	s_mov_b32 m0, s63
	v_mov_b32_e32 v155, v141
	global_load_lds_dwordx4 v[238:239], off
	v_lshl_add_u64 v[238:239], s[64:65], 0, v[138:139]
	s_add_i32 m0, s63, 0x2000
	s_nop 0
	global_load_lds_dwordx4 v[238:239], off
	s_mov_b32 m0, s5
	v_lshl_add_u64 v[238:239], s[46:47], 0, v[140:141]
	global_load_lds_dwordx4 v140, s[46:47]
	s_mov_b32 m0, s6
	s_nop 0
	global_load_lds_dwordx4 v154, s[46:47]
	s_waitcnt vmcnt(8)
	s_waitcnt lgkmcnt(0)
	v_lshl_add_u64 v[154:155], s[46:47], 0, v[154:155]
	s_barrier
	s_setprio 1
	v_mfma_f32_16x16x32_bf16 v[28:31], v[170:173], v[202:205], v[28:31]
	v_mfma_f32_16x16x32_bf16 v[24:27], v[178:181], v[202:205], v[24:27]
	v_mfma_f32_16x16x32_bf16 v[20:23], v[170:173], v[210:213], v[20:23]
	v_mfma_f32_16x16x32_bf16 v[16:19], v[178:181], v[210:213], v[16:19]
	v_mfma_f32_16x16x32_bf16 v[12:15], v[170:173], v[218:221], v[12:15]
	v_mfma_f32_16x16x32_bf16 v[8:11], v[178:181], v[218:221], v[8:11]
	v_mfma_f32_16x16x32_bf16 v[4:7], v[170:173], v[226:229], v[4:7]
	v_mfma_f32_16x16x32_bf16 v[0:3], v[178:181], v[226:229], v[0:3]
	v_mfma_f32_16x16x32_bf16 v[28:31], v[174:177], v[206:209], v[28:31]
	v_mfma_f32_16x16x32_bf16 v[24:27], v[182:185], v[206:209], v[24:27]
	v_mfma_f32_16x16x32_bf16 v[20:23], v[174:177], v[214:217], v[20:23]
	v_mfma_f32_16x16x32_bf16 v[16:19], v[182:185], v[214:217], v[16:19]
	v_mfma_f32_16x16x32_bf16 v[12:15], v[174:177], v[222:225], v[12:15]
	v_mfma_f32_16x16x32_bf16 v[8:11], v[182:185], v[222:225], v[8:11]
	v_mfma_f32_16x16x32_bf16 v[4:7], v[174:177], v[230:233], v[4:7]
	v_mfma_f32_16x16x32_bf16 v[0:3], v[182:185], v[230:233], v[0:3]
	s_setprio 0
	s_setprio 1
	v_mfma_f32_16x16x32_bf16 v[92:95], v[186:189], v[202:205], v[92:95]
	v_mfma_f32_16x16x32_bf16 v[88:91], v[194:197], v[202:205], v[88:91]
	v_mfma_f32_16x16x32_bf16 v[84:87], v[186:189], v[210:213], v[84:87]
	v_mfma_f32_16x16x32_bf16 v[80:83], v[194:197], v[210:213], v[80:83]
	v_mfma_f32_16x16x32_bf16 v[72:75], v[186:189], v[218:221], v[72:75]
	v_mfma_f32_16x16x32_bf16 v[76:79], v[194:197], v[218:221], v[76:79]
	v_mfma_f32_16x16x32_bf16 v[64:67], v[186:189], v[226:229], v[64:67]
	v_mfma_f32_16x16x32_bf16 v[68:71], v[194:197], v[226:229], v[68:71]
	v_mfma_f32_16x16x32_bf16 v[92:95], v[190:193], v[206:209], v[92:95]
	v_mfma_f32_16x16x32_bf16 v[88:91], v[198:201], v[206:209], v[88:91]
	v_mfma_f32_16x16x32_bf16 v[84:87], v[190:193], v[214:217], v[84:87]
	v_mfma_f32_16x16x32_bf16 v[80:83], v[198:201], v[214:217], v[80:83]
	v_mfma_f32_16x16x32_bf16 v[72:75], v[190:193], v[222:225], v[72:75]
	v_mfma_f32_16x16x32_bf16 v[76:79], v[198:201], v[222:225], v[76:79]
	v_mfma_f32_16x16x32_bf16 v[64:67], v[190:193], v[230:233], v[64:67]
	v_mfma_f32_16x16x32_bf16 v[68:71], v[198:201], v[230:233], v[68:71]
	s_setprio 0
	s_barrier
	s_add_i32 s63, 0, 0x18000
	v_add_u32_e32 v133, s63, v161
	s_add_i32 s64, 0, 0x1c000
	ds_read_b128 v[170:173], v133
	ds_read_b128 v[174:177], v133 offset:1024
	ds_read_b128 v[178:181], v133 offset:2048
	ds_read_b128 v[182:185], v133 offset:3072
	v_add_u32_e32 v133, s64, v161
	ds_read_b128 v[186:189], v133
	ds_read_b128 v[190:193], v133 offset:1024
	ds_read_b128 v[194:197], v133 offset:2048
	ds_read_b128 v[198:201], v133 offset:3072
	s_mov_b32 m0, s7
	ds_read_b128 v[202:205], v165 offset:32768
	ds_read_b128 v[206:209], v165 offset:33792
	ds_read_b128 v[210:213], v165 offset:34816
	ds_read_b128 v[214:217], v165 offset:35840
	ds_read_b128 v[218:221], v165 offset:36864
	ds_read_b128 v[222:225], v165 offset:37888
	ds_read_b128 v[226:229], v165 offset:38912
	ds_read_b128 v[230:233], v165 offset:39936
	global_load_lds_dwordx4 v129, s[46:47]
	s_mov_b32 m0, s31
	s_nop 0
	global_load_lds_dwordx4 v131, s[46:47]
	s_waitcnt vmcnt(8)
	s_waitcnt lgkmcnt(0)
	s_barrier
	s_setprio 1
	v_mfma_f32_16x16x32_bf16 v[60:63], v[170:173], v[202:205], v[60:63]
	v_mfma_f32_16x16x32_bf16 v[56:59], v[178:181], v[202:205], v[56:59]
	v_mfma_f32_16x16x32_bf16 v[52:55], v[170:173], v[210:213], v[52:55]
	v_mfma_f32_16x16x32_bf16 v[48:51], v[178:181], v[210:213], v[48:51]
	v_mfma_f32_16x16x32_bf16 v[44:47], v[170:173], v[218:221], v[44:47]
	v_mfma_f32_16x16x32_bf16 v[40:43], v[178:181], v[218:221], v[40:43]
	v_mfma_f32_16x16x32_bf16 v[36:39], v[170:173], v[226:229], v[36:39]
	v_mfma_f32_16x16x32_bf16 v[32:35], v[178:181], v[226:229], v[32:35]
	v_mfma_f32_16x16x32_bf16 v[60:63], v[174:177], v[206:209], v[60:63]
	v_mfma_f32_16x16x32_bf16 v[56:59], v[182:185], v[206:209], v[56:59]
	v_mfma_f32_16x16x32_bf16 v[52:55], v[174:177], v[214:217], v[52:55]
	v_mfma_f32_16x16x32_bf16 v[48:51], v[182:185], v[214:217], v[48:51]
	v_mfma_f32_16x16x32_bf16 v[44:47], v[174:177], v[222:225], v[44:47]
	v_mfma_f32_16x16x32_bf16 v[40:43], v[182:185], v[222:225], v[40:43]
	v_mfma_f32_16x16x32_bf16 v[36:39], v[174:177], v[230:233], v[36:39]
	v_mfma_f32_16x16x32_bf16 v[32:35], v[182:185], v[230:233], v[32:35]
	s_setprio 0
	s_setprio 1
	v_mfma_f32_16x16x32_bf16 v[124:127], v[186:189], v[202:205], v[124:127]
	v_mfma_f32_16x16x32_bf16 v[120:123], v[194:197], v[202:205], v[120:123]
	v_mfma_f32_16x16x32_bf16 v[116:119], v[186:189], v[210:213], v[116:119]
	v_mfma_f32_16x16x32_bf16 v[112:115], v[194:197], v[210:213], v[112:115]
	v_mfma_f32_16x16x32_bf16 v[108:111], v[186:189], v[218:221], v[108:111]
	v_mfma_f32_16x16x32_bf16 v[104:107], v[194:197], v[218:221], v[104:107]
	v_mfma_f32_16x16x32_bf16 v[100:103], v[186:189], v[226:229], v[100:103]
	v_mfma_f32_16x16x32_bf16 v[96:99], v[194:197], v[226:229], v[96:99]
	v_mfma_f32_16x16x32_bf16 v[124:127], v[190:193], v[206:209], v[124:127]
	v_mfma_f32_16x16x32_bf16 v[120:123], v[198:201], v[206:209], v[120:123]
	v_mfma_f32_16x16x32_bf16 v[116:119], v[190:193], v[214:217], v[116:119]
	v_mfma_f32_16x16x32_bf16 v[112:115], v[198:201], v[214:217], v[112:115]
	v_mfma_f32_16x16x32_bf16 v[108:111], v[190:193], v[222:225], v[108:111]
	v_mfma_f32_16x16x32_bf16 v[104:107], v[198:201], v[222:225], v[104:107]
	v_mfma_f32_16x16x32_bf16 v[100:103], v[190:193], v[230:233], v[100:103]
	v_mfma_f32_16x16x32_bf16 v[96:99], v[198:201], v[230:233], v[96:99]
	s_setprio 0
	s_barrier
	s_add_i32 s46, s63, s0
	v_lshl_add_u64 v[234:235], v[234:235], 0, s[24:25]
	s_mov_b32 m0, s46
	ds_read_b128 v[202:205], v165 offset:49152
	ds_read_b128 v[206:209], v165 offset:50176
	ds_read_b128 v[210:213], v165 offset:51200
	ds_read_b128 v[214:217], v165 offset:52224
	ds_read_b128 v[218:221], v165 offset:53248
	ds_read_b128 v[222:225], v165 offset:54272
	ds_read_b128 v[226:229], v165 offset:55296
	ds_read_b128 v[230:233], v165 offset:56320
	global_load_lds_dwordx4 v[234:235], off
	s_add_i32 m0, s46, 0x2000
	s_add_u32 s44, s44, 0x80080
	v_lshl_add_u64 v[234:235], v[236:237], 0, s[24:25]
	s_addc_u32 s45, s45, 0
	s_add_i32 s46, s64, s0
	global_load_lds_dwordx4 v[234:235], off
	v_lshl_add_u64 v[234:235], s[44:45], 0, v[136:137]
	s_mov_b32 m0, s46
	v_lshl_add_u64 v[154:155], v[154:155], 0, s[24:25]
	global_load_lds_dwordx4 v[234:235], off
	v_lshl_add_u64 v[234:235], s[44:45], 0, v[138:139]
	s_add_i32 m0, s46, 0x2000
	s_nop 0
	global_load_lds_dwordx4 v[234:235], off
	v_lshl_add_u64 v[234:235], v[238:239], 0, s[24:25]
	s_mov_b32 m0, s49
	s_nop 0
	global_load_lds_dwordx4 v[234:235], off
	s_mov_b32 m0, s51
	s_nop 0
	global_load_lds_dwordx4 v[154:155], off
	s_waitcnt vmcnt(8)
	s_waitcnt lgkmcnt(0)
	s_barrier
	s_setprio 1
	v_mfma_f32_16x16x32_bf16 v[28:31], v[170:173], v[202:205], v[28:31]
	v_mfma_f32_16x16x32_bf16 v[24:27], v[178:181], v[202:205], v[24:27]
	v_mfma_f32_16x16x32_bf16 v[20:23], v[170:173], v[210:213], v[20:23]
	v_mfma_f32_16x16x32_bf16 v[16:19], v[178:181], v[210:213], v[16:19]
	v_mfma_f32_16x16x32_bf16 v[12:15], v[170:173], v[218:221], v[12:15]
	v_mfma_f32_16x16x32_bf16 v[8:11], v[178:181], v[218:221], v[8:11]
	v_mfma_f32_16x16x32_bf16 v[4:7], v[170:173], v[226:229], v[4:7]
	v_mfma_f32_16x16x32_bf16 v[0:3], v[178:181], v[226:229], v[0:3]
	v_mfma_f32_16x16x32_bf16 v[28:31], v[174:177], v[206:209], v[28:31]
	v_mfma_f32_16x16x32_bf16 v[24:27], v[182:185], v[206:209], v[24:27]
	v_mfma_f32_16x16x32_bf16 v[20:23], v[174:177], v[214:217], v[20:23]
	v_mfma_f32_16x16x32_bf16 v[16:19], v[182:185], v[214:217], v[16:19]
	v_mfma_f32_16x16x32_bf16 v[12:15], v[174:177], v[222:225], v[12:15]
	v_mfma_f32_16x16x32_bf16 v[8:11], v[182:185], v[222:225], v[8:11]
	v_mfma_f32_16x16x32_bf16 v[4:7], v[174:177], v[230:233], v[4:7]
	v_mfma_f32_16x16x32_bf16 v[0:3], v[182:185], v[230:233], v[0:3]
	s_setprio 0
	s_setprio 1
	v_mfma_f32_16x16x32_bf16 v[92:95], v[186:189], v[202:205], v[92:95]
	v_mfma_f32_16x16x32_bf16 v[88:91], v[194:197], v[202:205], v[88:91]
	v_mfma_f32_16x16x32_bf16 v[84:87], v[186:189], v[210:213], v[84:87]
	v_mfma_f32_16x16x32_bf16 v[80:83], v[194:197], v[210:213], v[80:83]
	v_mfma_f32_16x16x32_bf16 v[72:75], v[186:189], v[218:221], v[72:75]
	v_mfma_f32_16x16x32_bf16 v[76:79], v[194:197], v[218:221], v[76:79]
	v_mfma_f32_16x16x32_bf16 v[64:67], v[186:189], v[226:229], v[64:67]
	v_mfma_f32_16x16x32_bf16 v[68:71], v[194:197], v[226:229], v[68:71]
	v_mfma_f32_16x16x32_bf16 v[92:95], v[190:193], v[206:209], v[92:95]
	v_mfma_f32_16x16x32_bf16 v[88:91], v[198:201], v[206:209], v[88:91]
	v_mfma_f32_16x16x32_bf16 v[84:87], v[190:193], v[214:217], v[84:87]
	v_mfma_f32_16x16x32_bf16 v[80:83], v[198:201], v[214:217], v[80:83]
	v_mfma_f32_16x16x32_bf16 v[72:75], v[190:193], v[222:225], v[72:75]
	v_mfma_f32_16x16x32_bf16 v[76:79], v[198:201], v[222:225], v[76:79]
	v_mfma_f32_16x16x32_bf16 v[64:67], v[190:193], v[230:233], v[64:67]
	v_mfma_f32_16x16x32_bf16 v[68:71], v[198:201], v[230:233], v[68:71]
	s_setprio 0
	s_barrier
	s_add_i32 s62, s62, 2
	s_add_u32 s10, s10, 0x100
	s_addc_u32 s11, s11, 0
	s_cmp_gt_u32 s62, 29
	s_cbranch_scc0 .LBB0_1571
	s_and_b64 vcc, exec, s[26:27]
	s_cbranch_vccnz .LBB0_1575
	v_lshl_add_u32 v150, s61, 8, v160
	s_cmp_lg_u32 s12, 46
	s_mov_b64 s[10:11], -1
	s_cbranch_scc1 .LBB0_1576

.LBB0_2279:
	s_add_i32 s65, s30, 2
	s_add_u32 s31, s24, s28
	s_addc_u32 s34, s25, s29
	v_add_u32_e32 v131, s46, v152
	s_add_u32 s66, s31, 0x100
	ds_read_b128 v[160:163], v131
	ds_read_b128 v[164:167], v131 offset:1024
	ds_read_b128 v[168:171], v131 offset:2048
	ds_read_b128 v[172:175], v131 offset:3072
	v_add_u32_e32 v131, s47, v152
	s_addc_u32 s34, s34, 0
	ds_read_b128 v[176:179], v131
	ds_read_b128 v[180:183], v131 offset:1024
	ds_read_b128 v[184:187], v131 offset:2048
	ds_read_b128 v[188:191], v131 offset:3072
	s_add_u32 s67, s63, s28
	s_addc_u32 s68, s64, s29
	s_cmp_eq_u32 s62, s30
	s_cselect_b64 vcc, -1, 0
	s_and_b64 s[30:31], vcc, exec
	s_cselect_b32 s30, s59, s67
	v_cndmask_b32_e32 v136, v128, v156, vcc
	s_cselect_b32 s35, s60, s34
	s_cselect_b32 s34, s61, s66
	v_cndmask_b32_e32 v129, v138, v158, vcc
	v_cndmask_b32_e32 v224, v130, v157, vcc
	v_cndmask_b32_e32 v131, v140, v159, vcc
	s_cselect_b32 s31, s19, s68
	v_lshl_add_u64 v[226:227], v[146:147], 0, s[28:29]
	s_add_i32 m0, s36, 0xc000
	ds_read_b128 v[192:195], v155
	ds_read_b128 v[196:199], v155 offset:1024
	ds_read_b128 v[200:203], v155 offset:2048
	ds_read_b128 v[204:207], v155 offset:3072
	ds_read_b128 v[208:211], v155 offset:4096
	ds_read_b128 v[212:215], v155 offset:5120
	ds_read_b128 v[216:219], v155 offset:6144
	ds_read_b128 v[220:223], v155 offset:7168
	global_load_lds_dwordx4 v[226:227], off
	v_lshl_add_u64 v[226:227], v[142:143], 0, s[28:29]
	s_add_i32 m0, s36, 0xe000
	s_nop 0
	global_load_lds_dwordx4 v[226:227], off
	s_waitcnt vmcnt(8)
	s_waitcnt lgkmcnt(0)
	s_barrier
	s_setprio 1
	v_mfma_f32_16x16x32_bf16 v[108:111], v[160:163], v[192:195], v[108:111]
	v_mfma_f32_16x16x32_bf16 v[104:107], v[168:171], v[192:195], v[104:107]
	v_mfma_f32_16x16x32_bf16 v[100:103], v[160:163], v[200:203], v[100:103]
	v_mfma_f32_16x16x32_bf16 v[96:99], v[168:171], v[200:203], v[96:99]
	v_mfma_f32_16x16x32_bf16 v[92:95], v[160:163], v[208:211], v[92:95]
	v_mfma_f32_16x16x32_bf16 v[88:91], v[168:171], v[208:211], v[88:91]
	v_mfma_f32_16x16x32_bf16 v[84:87], v[160:163], v[216:219], v[84:87]
	v_mfma_f32_16x16x32_bf16 v[80:83], v[168:171], v[216:219], v[80:83]
	v_mfma_f32_16x16x32_bf16 v[108:111], v[164:167], v[196:199], v[108:111]
	v_mfma_f32_16x16x32_bf16 v[104:107], v[172:175], v[196:199], v[104:107]
	v_mfma_f32_16x16x32_bf16 v[100:103], v[164:167], v[204:207], v[100:103]
	v_mfma_f32_16x16x32_bf16 v[96:99], v[172:175], v[204:207], v[96:99]
	v_mfma_f32_16x16x32_bf16 v[92:95], v[164:167], v[212:215], v[92:95]
	v_mfma_f32_16x16x32_bf16 v[88:91], v[172:175], v[212:215], v[88:91]
	v_mfma_f32_16x16x32_bf16 v[84:87], v[164:167], v[220:223], v[84:87]
	v_mfma_f32_16x16x32_bf16 v[80:83], v[172:175], v[220:223], v[80:83]
	s_setprio 0
	s_setprio 1
	v_mfma_f32_16x16x32_bf16 v[76:79], v[176:179], v[192:195], v[76:79]
	v_mfma_f32_16x16x32_bf16 v[72:75], v[184:187], v[192:195], v[72:75]
	v_mfma_f32_16x16x32_bf16 v[68:71], v[176:179], v[200:203], v[68:71]
	v_mfma_f32_16x16x32_bf16 v[64:67], v[184:187], v[200:203], v[64:67]
	v_mfma_f32_16x16x32_bf16 v[60:63], v[176:179], v[208:211], v[60:63]
	v_mfma_f32_16x16x32_bf16 v[56:59], v[184:187], v[208:211], v[56:59]
	v_mfma_f32_16x16x32_bf16 v[52:55], v[176:179], v[216:219], v[52:55]
	v_mfma_f32_16x16x32_bf16 v[48:51], v[184:187], v[216:219], v[48:51]
	v_mfma_f32_16x16x32_bf16 v[76:79], v[180:183], v[196:199], v[76:79]
	v_mfma_f32_16x16x32_bf16 v[72:75], v[188:191], v[196:199], v[72:75]
	v_mfma_f32_16x16x32_bf16 v[68:71], v[180:183], v[204:207], v[68:71]
	v_mfma_f32_16x16x32_bf16 v[64:67], v[188:191], v[204:207], v[64:67]
	v_mfma_f32_16x16x32_bf16 v[60:63], v[180:183], v[212:215], v[60:63]
	v_mfma_f32_16x16x32_bf16 v[56:59], v[188:191], v[212:215], v[56:59]
	v_mfma_f32_16x16x32_bf16 v[52:55], v[180:183], v[220:223], v[52:55]
	v_mfma_f32_16x16x32_bf16 v[48:51], v[188:191], v[220:223], v[48:51]
	s_setprio 0
	s_barrier
	s_add_i32 s66, s46, s5
	v_lshl_add_u64 v[226:227], s[30:31], 0, v[132:133]
	s_mov_b32 m0, s66
	ds_read_b128 v[192:195], v155 offset:16384
	ds_read_b128 v[196:199], v155 offset:17408
	ds_read_b128 v[200:203], v155 offset:18432
	ds_read_b128 v[204:207], v155 offset:19456
	ds_read_b128 v[208:211], v155 offset:20480
	ds_read_b128 v[212:215], v155 offset:21504
	ds_read_b128 v[216:219], v155 offset:22528
	ds_read_b128 v[220:223], v155 offset:23552
	global_load_lds_dwordx4 v[226:227], off
	s_add_i32 m0, s66, 0x2000
	s_add_u32 s66, s30, 0x80000
	v_lshl_add_u64 v[228:229], s[30:31], 0, v[134:135]
	s_addc_u32 s67, s31, 0
	s_add_i32 s68, s47, s5
	global_load_lds_dwordx4 v[228:229], off
	v_lshl_add_u64 v[230:231], s[66:67], 0, v[132:133]
	s_mov_b32 m0, s68
	v_mov_b32_e32 v225, v137
	global_load_lds_dwordx4 v[230:231], off
	v_lshl_add_u64 v[230:231], s[66:67], 0, v[134:135]
	s_add_i32 m0, s68, 0x2000
	s_nop 0
	global_load_lds_dwordx4 v[230:231], off
	s_mov_b32 m0, s36
	v_lshl_add_u64 v[230:231], s[34:35], 0, v[136:137]
	global_load_lds_dwordx4 v136, s[34:35]
	s_mov_b32 m0, s37
	s_nop 0
	global_load_lds_dwordx4 v224, s[34:35]
	s_waitcnt vmcnt(8)
	s_waitcnt lgkmcnt(0)
	v_lshl_add_u64 v[224:225], s[34:35], 0, v[224:225]
	s_barrier
	s_setprio 1
	v_mfma_f32_16x16x32_bf16 v[44:47], v[160:163], v[192:195], v[44:47]
	v_mfma_f32_16x16x32_bf16 v[40:43], v[168:171], v[192:195], v[40:43]
	v_mfma_f32_16x16x32_bf16 v[36:39], v[160:163], v[200:203], v[36:39]
	v_mfma_f32_16x16x32_bf16 v[32:35], v[168:171], v[200:203], v[32:35]
	v_mfma_f32_16x16x32_bf16 v[28:31], v[160:163], v[208:211], v[28:31]
	v_mfma_f32_16x16x32_bf16 v[24:27], v[168:171], v[208:211], v[24:27]
	v_mfma_f32_16x16x32_bf16 v[20:23], v[160:163], v[216:219], v[20:23]
	v_mfma_f32_16x16x32_bf16 v[16:19], v[168:171], v[216:219], v[16:19]
	v_mfma_f32_16x16x32_bf16 v[44:47], v[164:167], v[196:199], v[44:47]
	v_mfma_f32_16x16x32_bf16 v[40:43], v[172:175], v[196:199], v[40:43]
	v_mfma_f32_16x16x32_bf16 v[36:39], v[164:167], v[204:207], v[36:39]
	v_mfma_f32_16x16x32_bf16 v[32:35], v[172:175], v[204:207], v[32:35]
	v_mfma_f32_16x16x32_bf16 v[28:31], v[164:167], v[212:215], v[28:31]
	v_mfma_f32_16x16x32_bf16 v[24:27], v[172:175], v[212:215], v[24:27]
	v_mfma_f32_16x16x32_bf16 v[20:23], v[164:167], v[220:223], v[20:23]
	v_mfma_f32_16x16x32_bf16 v[16:19], v[172:175], v[220:223], v[16:19]
	s_setprio 0
	s_setprio 1
	v_mfma_f32_16x16x32_bf16 v[12:15], v[176:179], v[192:195], v[12:15]
	v_mfma_f32_16x16x32_bf16 v[8:11], v[184:187], v[192:195], v[8:11]
	v_mfma_f32_16x16x32_bf16 v[4:7], v[176:179], v[200:203], v[4:7]
	v_mfma_f32_16x16x32_bf16 v[0:3], v[184:187], v[200:203], v[0:3]
	v_mfma_f32_16x16x32_bf16 v[112:115], v[176:179], v[208:211], v[112:115]
	v_mfma_f32_16x16x32_bf16 v[116:119], v[184:187], v[208:211], v[116:119]
	v_mfma_f32_16x16x32_bf16 v[120:123], v[176:179], v[216:219], v[120:123]
	v_mfma_f32_16x16x32_bf16 v[124:127], v[184:187], v[216:219], v[124:127]
	v_mfma_f32_16x16x32_bf16 v[12:15], v[180:183], v[196:199], v[12:15]
	v_mfma_f32_16x16x32_bf16 v[8:11], v[188:191], v[196:199], v[8:11]
	v_mfma_f32_16x16x32_bf16 v[4:7], v[180:183], v[204:207], v[4:7]
	v_mfma_f32_16x16x32_bf16 v[0:3], v[188:191], v[204:207], v[0:3]
	v_mfma_f32_16x16x32_bf16 v[112:115], v[180:183], v[212:215], v[112:115]
	v_mfma_f32_16x16x32_bf16 v[116:119], v[188:191], v[212:215], v[116:119]
	v_mfma_f32_16x16x32_bf16 v[120:123], v[180:183], v[220:223], v[120:123]
	v_mfma_f32_16x16x32_bf16 v[124:127], v[188:191], v[220:223], v[124:127]
	s_setprio 0
	s_barrier
	s_add_i32 s66, 0, 0x18000
	v_add_u32_e32 v136, s66, v152
	s_add_i32 s67, 0, 0x1c000
	ds_read_b128 v[160:163], v136
	ds_read_b128 v[164:167], v136 offset:1024
	ds_read_b128 v[168:171], v136 offset:2048
	ds_read_b128 v[172:175], v136 offset:3072
	v_add_u32_e32 v136, s67, v152
	ds_read_b128 v[176:179], v136
	ds_read_b128 v[180:183], v136 offset:1024
	ds_read_b128 v[184:187], v136 offset:2048
	ds_read_b128 v[188:191], v136 offset:3072
	s_mov_b32 m0, s38
	ds_read_b128 v[192:195], v155 offset:32768
	ds_read_b128 v[196:199], v155 offset:33792
	ds_read_b128 v[200:203], v155 offset:34816
	ds_read_b128 v[204:207], v155 offset:35840
	ds_read_b128 v[208:211], v155 offset:36864
	ds_read_b128 v[212:215], v155 offset:37888
	ds_read_b128 v[216:219], v155 offset:38912
	ds_read_b128 v[220:223], v155 offset:39936
	global_load_lds_dwordx4 v129, s[34:35]
	s_mov_b32 m0, s39
	s_nop 0
	global_load_lds_dwordx4 v131, s[34:35]
	s_waitcnt vmcnt(8)
	s_waitcnt lgkmcnt(0)
	s_barrier
	s_setprio 1
	v_mfma_f32_16x16x32_bf16 v[108:111], v[160:163], v[192:195], v[108:111]
	v_mfma_f32_16x16x32_bf16 v[104:107], v[168:171], v[192:195], v[104:107]
	v_mfma_f32_16x16x32_bf16 v[100:103], v[160:163], v[200:203], v[100:103]
	v_mfma_f32_16x16x32_bf16 v[96:99], v[168:171], v[200:203], v[96:99]
	v_mfma_f32_16x16x32_bf16 v[92:95], v[160:163], v[208:211], v[92:95]
	v_mfma_f32_16x16x32_bf16 v[88:91], v[168:171], v[208:211], v[88:91]
	v_mfma_f32_16x16x32_bf16 v[84:87], v[160:163], v[216:219], v[84:87]
	v_mfma_f32_16x16x32_bf16 v[80:83], v[168:171], v[216:219], v[80:83]
	v_mfma_f32_16x16x32_bf16 v[108:111], v[164:167], v[196:199], v[108:111]
	v_mfma_f32_16x16x32_bf16 v[104:107], v[172:175], v[196:199], v[104:107]
	v_mfma_f32_16x16x32_bf16 v[100:103], v[164:167], v[204:207], v[100:103]
	v_mfma_f32_16x16x32_bf16 v[96:99], v[172:175], v[204:207], v[96:99]
	v_mfma_f32_16x16x32_bf16 v[92:95], v[164:167], v[212:215], v[92:95]
	v_mfma_f32_16x16x32_bf16 v[88:91], v[172:175], v[212:215], v[88:91]
	v_mfma_f32_16x16x32_bf16 v[84:87], v[164:167], v[220:223], v[84:87]
	v_mfma_f32_16x16x32_bf16 v[80:83], v[172:175], v[220:223], v[80:83]
	s_setprio 0
	s_setprio 1
	v_mfma_f32_16x16x32_bf16 v[76:79], v[176:179], v[192:195], v[76:79]
	v_mfma_f32_16x16x32_bf16 v[72:75], v[184:187], v[192:195], v[72:75]
	v_mfma_f32_16x16x32_bf16 v[68:71], v[176:179], v[200:203], v[68:71]
	v_mfma_f32_16x16x32_bf16 v[64:67], v[184:187], v[200:203], v[64:67]
	v_mfma_f32_16x16x32_bf16 v[60:63], v[176:179], v[208:211], v[60:63]
	v_mfma_f32_16x16x32_bf16 v[56:59], v[184:187], v[208:211], v[56:59]
	v_mfma_f32_16x16x32_bf16 v[52:55], v[176:179], v[216:219], v[52:55]
	v_mfma_f32_16x16x32_bf16 v[48:51], v[184:187], v[216:219], v[48:51]
	v_mfma_f32_16x16x32_bf16 v[76:79], v[180:183], v[196:199], v[76:79]
	v_mfma_f32_16x16x32_bf16 v[72:75], v[188:191], v[196:199], v[72:75]
	v_mfma_f32_16x16x32_bf16 v[68:71], v[180:183], v[204:207], v[68:71]
	v_mfma_f32_16x16x32_bf16 v[64:67], v[188:191], v[204:207], v[64:67]
	v_mfma_f32_16x16x32_bf16 v[60:63], v[180:183], v[212:215], v[60:63]
	v_mfma_f32_16x16x32_bf16 v[56:59], v[188:191], v[212:215], v[56:59]
	v_mfma_f32_16x16x32_bf16 v[52:55], v[180:183], v[220:223], v[52:55]
	v_mfma_f32_16x16x32_bf16 v[48:51], v[188:191], v[220:223], v[48:51]
	s_setprio 0
	s_barrier
	s_add_i32 s34, s66, s5
	v_lshl_add_u64 v[226:227], v[226:227], 0, s[12:13]
	s_mov_b32 m0, s34
	ds_read_b128 v[192:195], v155 offset:49152
	ds_read_b128 v[196:199], v155 offset:50176
	ds_read_b128 v[200:203], v155 offset:51200
	ds_read_b128 v[204:207], v155 offset:52224
	ds_read_b128 v[208:211], v155 offset:53248
	ds_read_b128 v[212:215], v155 offset:54272
	ds_read_b128 v[216:219], v155 offset:55296
	ds_read_b128 v[220:223], v155 offset:56320
	global_load_lds_dwordx4 v[226:227], off
	s_add_i32 m0, s34, 0x2000
	s_add_u32 s30, s30, 0x80080
	v_lshl_add_u64 v[226:227], v[228:229], 0, s[12:13]
	s_addc_u32 s31, s31, 0
	s_add_i32 s34, s67, s5
	global_load_lds_dwordx4 v[226:227], off
	v_lshl_add_u64 v[226:227], s[30:31], 0, v[132:133]
	s_mov_b32 m0, s34
	v_lshl_add_u64 v[224:225], v[224:225], 0, s[12:13]
	global_load_lds_dwordx4 v[226:227], off
	v_lshl_add_u64 v[226:227], s[30:31], 0, v[134:135]
	s_add_i32 m0, s34, 0x2000
	s_nop 0
	global_load_lds_dwordx4 v[226:227], off
	v_lshl_add_u64 v[226:227], v[230:231], 0, s[12:13]
	s_mov_b32 m0, s42
	s_nop 0
	global_load_lds_dwordx4 v[226:227], off
	s_mov_b32 m0, s43
	s_nop 0
	global_load_lds_dwordx4 v[224:225], off
	s_waitcnt vmcnt(8)
	s_waitcnt lgkmcnt(0)
	s_barrier
	s_setprio 1
	v_mfma_f32_16x16x32_bf16 v[44:47], v[160:163], v[192:195], v[44:47]
	v_mfma_f32_16x16x32_bf16 v[40:43], v[168:171], v[192:195], v[40:43]
	v_mfma_f32_16x16x32_bf16 v[36:39], v[160:163], v[200:203], v[36:39]
	v_mfma_f32_16x16x32_bf16 v[32:35], v[168:171], v[200:203], v[32:35]
	v_mfma_f32_16x16x32_bf16 v[28:31], v[160:163], v[208:211], v[28:31]
	v_mfma_f32_16x16x32_bf16 v[24:27], v[168:171], v[208:211], v[24:27]
	v_mfma_f32_16x16x32_bf16 v[20:23], v[160:163], v[216:219], v[20:23]
	v_mfma_f32_16x16x32_bf16 v[16:19], v[168:171], v[216:219], v[16:19]
	v_mfma_f32_16x16x32_bf16 v[44:47], v[164:167], v[196:199], v[44:47]
	v_mfma_f32_16x16x32_bf16 v[40:43], v[172:175], v[196:199], v[40:43]
	v_mfma_f32_16x16x32_bf16 v[36:39], v[164:167], v[204:207], v[36:39]
	v_mfma_f32_16x16x32_bf16 v[32:35], v[172:175], v[204:207], v[32:35]
	v_mfma_f32_16x16x32_bf16 v[28:31], v[164:167], v[212:215], v[28:31]
	v_mfma_f32_16x16x32_bf16 v[24:27], v[172:175], v[212:215], v[24:27]
	v_mfma_f32_16x16x32_bf16 v[20:23], v[164:167], v[220:223], v[20:23]
	v_mfma_f32_16x16x32_bf16 v[16:19], v[172:175], v[220:223], v[16:19]
	s_setprio 0
	s_setprio 1
	v_mfma_f32_16x16x32_bf16 v[12:15], v[176:179], v[192:195], v[12:15]
	v_mfma_f32_16x16x32_bf16 v[8:11], v[184:187], v[192:195], v[8:11]
	v_mfma_f32_16x16x32_bf16 v[4:7], v[176:179], v[200:203], v[4:7]
	v_mfma_f32_16x16x32_bf16 v[0:3], v[184:187], v[200:203], v[0:3]
	v_mfma_f32_16x16x32_bf16 v[112:115], v[176:179], v[208:211], v[112:115]
	v_mfma_f32_16x16x32_bf16 v[116:119], v[184:187], v[208:211], v[116:119]
	v_mfma_f32_16x16x32_bf16 v[120:123], v[176:179], v[216:219], v[120:123]
	v_mfma_f32_16x16x32_bf16 v[124:127], v[184:187], v[216:219], v[124:127]
	v_mfma_f32_16x16x32_bf16 v[12:15], v[180:183], v[196:199], v[12:15]
	v_mfma_f32_16x16x32_bf16 v[8:11], v[188:191], v[196:199], v[8:11]
	v_mfma_f32_16x16x32_bf16 v[4:7], v[180:183], v[204:207], v[4:7]
	v_mfma_f32_16x16x32_bf16 v[0:3], v[188:191], v[204:207], v[0:3]
	v_mfma_f32_16x16x32_bf16 v[112:115], v[180:183], v[212:215], v[112:115]
	v_mfma_f32_16x16x32_bf16 v[116:119], v[188:191], v[212:215], v[116:119]
	v_mfma_f32_16x16x32_bf16 v[120:123], v[180:183], v[220:223], v[120:123]
	v_mfma_f32_16x16x32_bf16 v[124:127], v[188:191], v[220:223], v[124:127]
	s_setprio 0
	s_barrier
	s_add_u32 s28, s28, 0x100
	s_addc_u32 s29, s29, 0
	s_cmp_ge_i32 s65, s57
	s_mov_b32 s30, s65
	s_cbranch_scc0 .LBB0_2279
	s_and_b64 vcc, exec, s[14:15]
	s_cbranch_vccz .LBB0_2282
	s_barrier

.LBB0_2355:
	ds_read_b128 v[140:143], v162
	ds_read_b128 v[170:173], v162 offset:1024
	ds_read_b128 v[174:177], v162 offset:2048
	ds_read_b128 v[178:181], v162 offset:3072
	ds_read_b128 v[182:185], v163
	ds_read_b128 v[186:189], v163 offset:1024
	ds_read_b128 v[190:193], v163 offset:2048
	ds_read_b128 v[194:197], v163 offset:3072
	s_add_u32 s42, s38, s8
	s_addc_u32 s43, s39, s9
	s_cmpk_eq_i32 s8, 0x1000
	s_cselect_b64 vcc, -1, 0
	s_and_b64 s[40:41], vcc, exec
	s_cselect_b32 s68, 0, s8
	s_cselect_b32 s67, 0, s9
	s_cselect_b32 s40, s65, s42
	s_cselect_b32 s41, s35, s43
	s_add_u32 s42, s10, s68
	v_cndmask_b32_e32 v150, v128, v165, vcc
	v_cndmask_b32_e32 v129, v132, v167, vcc
	v_cndmask_b32_e32 v230, v130, v166, vcc
	v_cndmask_b32_e32 v131, v134, v168, vcc
	s_addc_u32 s43, s11, s67
	v_lshl_add_u64 v[232:233], v[138:139], 0, s[8:9]
	v_lshl_add_u64 v[232:233], v[232:233], 0, s[24:25]
	s_add_i32 m0, s44, 0xc000
	ds_read_b128 v[198:201], v164
	ds_read_b128 v[202:205], v164 offset:1024
	ds_read_b128 v[206:209], v164 offset:2048
	ds_read_b128 v[210:213], v164 offset:3072
	ds_read_b128 v[214:217], v164 offset:4096
	ds_read_b128 v[218:221], v164 offset:5120
	ds_read_b128 v[222:225], v164 offset:6144
	ds_read_b128 v[226:229], v164 offset:7168
	global_load_lds_dwordx4 v[232:233], off
	v_lshl_add_u64 v[232:233], v[136:137], 0, s[8:9]
	v_lshl_add_u64 v[232:233], v[232:233], 0, s[24:25]
	s_add_i32 m0, s44, 0xe000
	s_nop 0
	global_load_lds_dwordx4 v[232:233], off
	s_waitcnt vmcnt(8)
	s_waitcnt lgkmcnt(0)
	s_barrier
	s_setprio 1
	v_mfma_f32_16x16x32_bf16 v[124:127], v[140:143], v[198:201], v[124:127]
	v_mfma_f32_16x16x32_bf16 v[120:123], v[174:177], v[198:201], v[120:123]
	v_mfma_f32_16x16x32_bf16 v[116:119], v[140:143], v[206:209], v[116:119]
	v_mfma_f32_16x16x32_bf16 v[112:115], v[174:177], v[206:209], v[112:115]
	v_mfma_f32_16x16x32_bf16 v[108:111], v[140:143], v[214:217], v[108:111]
	v_mfma_f32_16x16x32_bf16 v[100:103], v[174:177], v[214:217], v[100:103]
	v_mfma_f32_16x16x32_bf16 v[92:95], v[140:143], v[222:225], v[92:95]
	v_mfma_f32_16x16x32_bf16 v[84:87], v[174:177], v[222:225], v[84:87]
	v_mfma_f32_16x16x32_bf16 v[124:127], v[170:173], v[202:205], v[124:127]
	v_mfma_f32_16x16x32_bf16 v[120:123], v[178:181], v[202:205], v[120:123]
	v_mfma_f32_16x16x32_bf16 v[116:119], v[170:173], v[210:213], v[116:119]
	v_mfma_f32_16x16x32_bf16 v[112:115], v[178:181], v[210:213], v[112:115]
	v_mfma_f32_16x16x32_bf16 v[108:111], v[170:173], v[218:221], v[108:111]
	v_mfma_f32_16x16x32_bf16 v[100:103], v[178:181], v[218:221], v[100:103]
	v_mfma_f32_16x16x32_bf16 v[92:95], v[170:173], v[226:229], v[92:95]
	v_mfma_f32_16x16x32_bf16 v[84:87], v[178:181], v[226:229], v[84:87]
	s_setprio 0
	s_setprio 1
	v_mfma_f32_16x16x32_bf16 v[104:107], v[182:185], v[198:201], v[104:107]
	v_mfma_f32_16x16x32_bf16 v[96:99], v[190:193], v[198:201], v[96:99]
	v_mfma_f32_16x16x32_bf16 v[88:91], v[182:185], v[206:209], v[88:91]
	v_mfma_f32_16x16x32_bf16 v[80:83], v[190:193], v[206:209], v[80:83]
	v_mfma_f32_16x16x32_bf16 v[76:79], v[182:185], v[214:217], v[76:79]
	v_mfma_f32_16x16x32_bf16 v[72:75], v[190:193], v[214:217], v[72:75]
	v_mfma_f32_16x16x32_bf16 v[68:71], v[182:185], v[222:225], v[68:71]
	v_mfma_f32_16x16x32_bf16 v[64:67], v[190:193], v[222:225], v[64:67]
	v_mfma_f32_16x16x32_bf16 v[104:107], v[186:189], v[202:205], v[104:107]
	v_mfma_f32_16x16x32_bf16 v[96:99], v[194:197], v[202:205], v[96:99]
	v_mfma_f32_16x16x32_bf16 v[88:91], v[186:189], v[210:213], v[88:91]
	v_mfma_f32_16x16x32_bf16 v[80:83], v[194:197], v[210:213], v[80:83]
	v_mfma_f32_16x16x32_bf16 v[76:79], v[186:189], v[218:221], v[76:79]
	v_mfma_f32_16x16x32_bf16 v[72:75], v[194:197], v[218:221], v[72:75]
	v_mfma_f32_16x16x32_bf16 v[68:71], v[186:189], v[226:229], v[68:71]
	v_mfma_f32_16x16x32_bf16 v[64:67], v[194:197], v[226:229], v[64:67]
	s_setprio 0
	s_barrier
	s_add_i32 s67, s53, s5
	v_lshl_add_u64 v[232:233], s[40:41], 0, v[146:147]
	s_mov_b32 m0, s67
	ds_read_b128 v[198:201], v164 offset:16384
	ds_read_b128 v[202:205], v164 offset:17408
	ds_read_b128 v[206:209], v164 offset:18432
	ds_read_b128 v[210:213], v164 offset:19456
	ds_read_b128 v[214:217], v164 offset:20480
	ds_read_b128 v[218:221], v164 offset:21504
	ds_read_b128 v[222:225], v164 offset:22528
	ds_read_b128 v[226:229], v164 offset:23552
	global_load_lds_dwordx4 v[232:233], off
	s_add_i32 m0, s67, 0x2000
	s_add_u32 s68, s40, 0x80000
	v_lshl_add_u64 v[234:235], s[40:41], 0, v[148:149]
	s_addc_u32 s69, s41, 0
	s_add_i32 s67, s55, s5
	global_load_lds_dwordx4 v[234:235], off
	v_lshl_add_u64 v[236:237], s[68:69], 0, v[146:147]
	s_mov_b32 m0, s67
	v_mov_b32_e32 v231, v151
	global_load_lds_dwordx4 v[236:237], off
	v_lshl_add_u64 v[236:237], s[68:69], 0, v[148:149]
	s_add_i32 m0, s67, 0x2000
	s_nop 0
	global_load_lds_dwordx4 v[236:237], off
	s_mov_b32 m0, s44
	v_lshl_add_u64 v[236:237], s[42:43], 0, v[150:151]
	global_load_lds_dwordx4 v150, s[42:43]
	s_mov_b32 m0, s45
	s_nop 0
	global_load_lds_dwordx4 v230, s[42:43]
	s_waitcnt vmcnt(8)
	s_waitcnt lgkmcnt(0)
	v_lshl_add_u64 v[230:231], s[42:43], 0, v[230:231]
	s_barrier
	s_setprio 1
	v_mfma_f32_16x16x32_bf16 v[60:63], v[140:143], v[198:201], v[60:63]
	v_mfma_f32_16x16x32_bf16 v[56:59], v[174:177], v[198:201], v[56:59]
	v_mfma_f32_16x16x32_bf16 v[44:47], v[140:143], v[206:209], v[44:47]
	v_mfma_f32_16x16x32_bf16 v[36:39], v[174:177], v[206:209], v[36:39]
	v_mfma_f32_16x16x32_bf16 v[20:23], v[140:143], v[214:217], v[20:23]
	v_mfma_f32_16x16x32_bf16 v[12:15], v[174:177], v[214:217], v[12:15]
	v_mfma_f32_16x16x32_bf16 v[4:7], v[140:143], v[222:225], v[4:7]
	v_mfma_f32_16x16x32_bf16 v[0:3], v[174:177], v[222:225], v[0:3]
	v_mfma_f32_16x16x32_bf16 v[60:63], v[170:173], v[202:205], v[60:63]
	v_mfma_f32_16x16x32_bf16 v[56:59], v[178:181], v[202:205], v[56:59]
	v_mfma_f32_16x16x32_bf16 v[44:47], v[170:173], v[210:213], v[44:47]
	v_mfma_f32_16x16x32_bf16 v[36:39], v[178:181], v[210:213], v[36:39]
	v_mfma_f32_16x16x32_bf16 v[20:23], v[170:173], v[218:221], v[20:23]
	v_mfma_f32_16x16x32_bf16 v[12:15], v[178:181], v[218:221], v[12:15]
	v_mfma_f32_16x16x32_bf16 v[4:7], v[170:173], v[226:229], v[4:7]
	v_mfma_f32_16x16x32_bf16 v[0:3], v[178:181], v[226:229], v[0:3]
	s_setprio 0
	s_setprio 1
	v_mfma_f32_16x16x32_bf16 v[40:43], v[182:185], v[198:201], v[40:43]
	v_mfma_f32_16x16x32_bf16 v[32:35], v[190:193], v[198:201], v[32:35]
	v_mfma_f32_16x16x32_bf16 v[16:19], v[182:185], v[206:209], v[16:19]
	v_mfma_f32_16x16x32_bf16 v[8:11], v[190:193], v[206:209], v[8:11]
	v_mfma_f32_16x16x32_bf16 v[48:51], v[182:185], v[214:217], v[48:51]
	v_mfma_f32_16x16x32_bf16 v[52:55], v[190:193], v[214:217], v[52:55]
	v_mfma_f32_16x16x32_bf16 v[24:27], v[182:185], v[222:225], v[24:27]
	v_mfma_f32_16x16x32_bf16 v[28:31], v[190:193], v[222:225], v[28:31]
	v_mfma_f32_16x16x32_bf16 v[40:43], v[186:189], v[202:205], v[40:43]
	v_mfma_f32_16x16x32_bf16 v[32:35], v[194:197], v[202:205], v[32:35]
	v_mfma_f32_16x16x32_bf16 v[16:19], v[186:189], v[210:213], v[16:19]
	v_mfma_f32_16x16x32_bf16 v[8:11], v[194:197], v[210:213], v[8:11]
	v_mfma_f32_16x16x32_bf16 v[48:51], v[186:189], v[218:221], v[48:51]
	v_mfma_f32_16x16x32_bf16 v[52:55], v[194:197], v[218:221], v[52:55]
	v_mfma_f32_16x16x32_bf16 v[24:27], v[186:189], v[226:229], v[24:27]
	v_mfma_f32_16x16x32_bf16 v[28:31], v[194:197], v[226:229], v[28:31]
	s_setprio 0
	s_barrier
	s_add_i32 s67, 0, 0x18000
	v_add_u32_e32 v133, s67, v160
	s_add_i32 s68, 0, 0x1c000
	ds_read_b128 v[140:143], v133
	ds_read_b128 v[170:173], v133 offset:1024
	ds_read_b128 v[174:177], v133 offset:2048
	ds_read_b128 v[178:181], v133 offset:3072
	v_add_u32_e32 v133, s68, v160
	ds_read_b128 v[182:185], v133
	ds_read_b128 v[186:189], v133 offset:1024
	ds_read_b128 v[190:193], v133 offset:2048
	ds_read_b128 v[194:197], v133 offset:3072
	s_mov_b32 m0, s46
	ds_read_b128 v[198:201], v164 offset:32768
	ds_read_b128 v[202:205], v164 offset:33792
	ds_read_b128 v[206:209], v164 offset:34816
	ds_read_b128 v[210:213], v164 offset:35840
	ds_read_b128 v[214:217], v164 offset:36864
	ds_read_b128 v[218:221], v164 offset:37888
	ds_read_b128 v[222:225], v164 offset:38912
	ds_read_b128 v[226:229], v164 offset:39936
	global_load_lds_dwordx4 v129, s[42:43]
	s_mov_b32 m0, s47
	s_nop 0
	global_load_lds_dwordx4 v131, s[42:43]
	s_waitcnt vmcnt(8)
	s_waitcnt lgkmcnt(0)
	s_barrier
	s_setprio 1
	v_mfma_f32_16x16x32_bf16 v[124:127], v[140:143], v[198:201], v[124:127]
	v_mfma_f32_16x16x32_bf16 v[120:123], v[174:177], v[198:201], v[120:123]
	v_mfma_f32_16x16x32_bf16 v[116:119], v[140:143], v[206:209], v[116:119]
	v_mfma_f32_16x16x32_bf16 v[112:115], v[174:177], v[206:209], v[112:115]
	v_mfma_f32_16x16x32_bf16 v[108:111], v[140:143], v[214:217], v[108:111]
	v_mfma_f32_16x16x32_bf16 v[100:103], v[174:177], v[214:217], v[100:103]
	v_mfma_f32_16x16x32_bf16 v[92:95], v[140:143], v[222:225], v[92:95]
	v_mfma_f32_16x16x32_bf16 v[84:87], v[174:177], v[222:225], v[84:87]
	v_mfma_f32_16x16x32_bf16 v[124:127], v[170:173], v[202:205], v[124:127]
	v_mfma_f32_16x16x32_bf16 v[120:123], v[178:181], v[202:205], v[120:123]
	v_mfma_f32_16x16x32_bf16 v[116:119], v[170:173], v[210:213], v[116:119]
	v_mfma_f32_16x16x32_bf16 v[112:115], v[178:181], v[210:213], v[112:115]
	v_mfma_f32_16x16x32_bf16 v[108:111], v[170:173], v[218:221], v[108:111]
	v_mfma_f32_16x16x32_bf16 v[100:103], v[178:181], v[218:221], v[100:103]
	v_mfma_f32_16x16x32_bf16 v[92:95], v[170:173], v[226:229], v[92:95]
	v_mfma_f32_16x16x32_bf16 v[84:87], v[178:181], v[226:229], v[84:87]
	s_setprio 0
	s_setprio 1
	v_mfma_f32_16x16x32_bf16 v[104:107], v[182:185], v[198:201], v[104:107]
	v_mfma_f32_16x16x32_bf16 v[96:99], v[190:193], v[198:201], v[96:99]
	v_mfma_f32_16x16x32_bf16 v[88:91], v[182:185], v[206:209], v[88:91]
	v_mfma_f32_16x16x32_bf16 v[80:83], v[190:193], v[206:209], v[80:83]
	v_mfma_f32_16x16x32_bf16 v[76:79], v[182:185], v[214:217], v[76:79]
	v_mfma_f32_16x16x32_bf16 v[72:75], v[190:193], v[214:217], v[72:75]
	v_mfma_f32_16x16x32_bf16 v[68:71], v[182:185], v[222:225], v[68:71]
	v_mfma_f32_16x16x32_bf16 v[64:67], v[190:193], v[222:225], v[64:67]
	v_mfma_f32_16x16x32_bf16 v[104:107], v[186:189], v[202:205], v[104:107]
	v_mfma_f32_16x16x32_bf16 v[96:99], v[194:197], v[202:205], v[96:99]
	v_mfma_f32_16x16x32_bf16 v[88:91], v[186:189], v[210:213], v[88:91]
	v_mfma_f32_16x16x32_bf16 v[80:83], v[194:197], v[210:213], v[80:83]
	v_mfma_f32_16x16x32_bf16 v[76:79], v[186:189], v[218:221], v[76:79]
	v_mfma_f32_16x16x32_bf16 v[72:75], v[194:197], v[218:221], v[72:75]
	v_mfma_f32_16x16x32_bf16 v[68:71], v[186:189], v[226:229], v[68:71]
	v_mfma_f32_16x16x32_bf16 v[64:67], v[194:197], v[226:229], v[64:67]
	s_setprio 0
	s_barrier
	s_add_i32 s42, s67, s5
	v_lshl_add_u64 v[232:233], v[232:233], 0, s[20:21]
	s_mov_b32 m0, s42
	ds_read_b128 v[198:201], v164 offset:49152
	ds_read_b128 v[202:205], v164 offset:50176
	ds_read_b128 v[206:209], v164 offset:51200
	ds_read_b128 v[210:213], v164 offset:52224
	ds_read_b128 v[214:217], v164 offset:53248
	ds_read_b128 v[218:221], v164 offset:54272
	ds_read_b128 v[222:225], v164 offset:55296
	ds_read_b128 v[226:229], v164 offset:56320
	global_load_lds_dwordx4 v[232:233], off
	s_add_i32 m0, s42, 0x2000
	s_add_u32 s40, s40, 0x80080
	v_lshl_add_u64 v[232:233], v[234:235], 0, s[20:21]
	s_addc_u32 s41, s41, 0
	s_add_i32 s42, s68, s5
	global_load_lds_dwordx4 v[232:233], off
	v_lshl_add_u64 v[232:233], s[40:41], 0, v[146:147]
	s_mov_b32 m0, s42
	v_lshl_add_u64 v[230:231], v[230:231], 0, s[20:21]
	global_load_lds_dwordx4 v[232:233], off
	v_lshl_add_u64 v[232:233], s[40:41], 0, v[148:149]
	s_add_i32 m0, s42, 0x2000
	s_nop 0
	global_load_lds_dwordx4 v[232:233], off
	v_lshl_add_u64 v[232:233], v[236:237], 0, s[20:21]
	s_mov_b32 m0, s49
	s_nop 0
	global_load_lds_dwordx4 v[232:233], off
	s_mov_b32 m0, s51
	s_nop 0
	global_load_lds_dwordx4 v[230:231], off
	s_waitcnt vmcnt(8)
	s_waitcnt lgkmcnt(0)
	s_barrier
	s_setprio 1
	v_mfma_f32_16x16x32_bf16 v[60:63], v[140:143], v[198:201], v[60:63]
	v_mfma_f32_16x16x32_bf16 v[56:59], v[174:177], v[198:201], v[56:59]
	v_mfma_f32_16x16x32_bf16 v[44:47], v[140:143], v[206:209], v[44:47]
	v_mfma_f32_16x16x32_bf16 v[36:39], v[174:177], v[206:209], v[36:39]
	v_mfma_f32_16x16x32_bf16 v[20:23], v[140:143], v[214:217], v[20:23]
	v_mfma_f32_16x16x32_bf16 v[12:15], v[174:177], v[214:217], v[12:15]
	v_mfma_f32_16x16x32_bf16 v[4:7], v[140:143], v[222:225], v[4:7]
	v_mfma_f32_16x16x32_bf16 v[0:3], v[174:177], v[222:225], v[0:3]
	v_mfma_f32_16x16x32_bf16 v[60:63], v[170:173], v[202:205], v[60:63]
	v_mfma_f32_16x16x32_bf16 v[56:59], v[178:181], v[202:205], v[56:59]
	v_mfma_f32_16x16x32_bf16 v[44:47], v[170:173], v[210:213], v[44:47]
	v_mfma_f32_16x16x32_bf16 v[36:39], v[178:181], v[210:213], v[36:39]
	v_mfma_f32_16x16x32_bf16 v[20:23], v[170:173], v[218:221], v[20:23]
	v_mfma_f32_16x16x32_bf16 v[12:15], v[178:181], v[218:221], v[12:15]
	v_mfma_f32_16x16x32_bf16 v[4:7], v[170:173], v[226:229], v[4:7]
	v_mfma_f32_16x16x32_bf16 v[0:3], v[178:181], v[226:229], v[0:3]
	s_setprio 0
	s_setprio 1
	v_mfma_f32_16x16x32_bf16 v[40:43], v[182:185], v[198:201], v[40:43]
	v_mfma_f32_16x16x32_bf16 v[32:35], v[190:193], v[198:201], v[32:35]
	v_mfma_f32_16x16x32_bf16 v[16:19], v[182:185], v[206:209], v[16:19]
	v_mfma_f32_16x16x32_bf16 v[8:11], v[190:193], v[206:209], v[8:11]
	v_mfma_f32_16x16x32_bf16 v[48:51], v[182:185], v[214:217], v[48:51]
	v_mfma_f32_16x16x32_bf16 v[52:55], v[190:193], v[214:217], v[52:55]
	v_mfma_f32_16x16x32_bf16 v[24:27], v[182:185], v[222:225], v[24:27]
	v_mfma_f32_16x16x32_bf16 v[28:31], v[190:193], v[222:225], v[28:31]
	v_mfma_f32_16x16x32_bf16 v[40:43], v[186:189], v[202:205], v[40:43]
	v_mfma_f32_16x16x32_bf16 v[32:35], v[194:197], v[202:205], v[32:35]
	v_mfma_f32_16x16x32_bf16 v[16:19], v[186:189], v[210:213], v[16:19]
	v_mfma_f32_16x16x32_bf16 v[8:11], v[194:197], v[210:213], v[8:11]
	v_mfma_f32_16x16x32_bf16 v[48:51], v[186:189], v[218:221], v[48:51]
	v_mfma_f32_16x16x32_bf16 v[52:55], v[194:197], v[218:221], v[52:55]
	v_mfma_f32_16x16x32_bf16 v[24:27], v[186:189], v[226:229], v[24:27]
	v_mfma_f32_16x16x32_bf16 v[28:31], v[194:197], v[226:229], v[28:31]
	s_setprio 0
	s_barrier
	s_add_i32 s66, s66, 2
	s_add_u32 s8, s8, 0x100
	s_addc_u32 s9, s9, 0
	s_cmp_gt_u32 s66, 29
	s_cbranch_scc0 .LBB0_2355
	s_and_b64 vcc, exec, s[22:23]
	s_cbranch_vccz .LBB0_2358
	s_barrier

.LBB0_2750:
	v_add_u32_e32 v163, s48, v143
	ds_read_b128 v[164:167], v163
	ds_read_b128 v[168:171], v163 offset:1024
	ds_read_b128 v[172:175], v163 offset:2048
	ds_read_b128 v[176:179], v163 offset:3072
	v_add_u32_e32 v163, s49, v143
	ds_read_b128 v[180:183], v163
	ds_read_b128 v[184:187], v163 offset:1024
	ds_read_b128 v[188:191], v163 offset:2048
	ds_read_b128 v[192:195], v163 offset:3072
	s_cmpk_eq_i32 s8, 0x1000
	s_cselect_b64 vcc, -1, 0
	s_and_b64 s[40:41], vcc, exec
	s_cselect_b32 s40, 0, s8
	v_lshl_add_u64 v[196:197], v[148:149], 0, s[8:9]
	s_cselect_b32 s41, 0, s9
	s_add_u32 s40, s18, s40
	v_cndmask_b32_e32 v132, v146, v158, vcc
	v_cndmask_b32_e32 v139, v140, v160, vcc
	v_cndmask_b32_e32 v228, v142, v159, vcc
	v_cndmask_b32_e32 v141, v138, v161, vcc
	v_cndmask_b32_e32 v230, v196, v162, vcc
	v_cndmask_b32_e32 v231, v197, v135, vcc
	s_addc_u32 s41, s19, s41
	v_lshl_add_u64 v[232:233], v[152:153], 0, s[8:9]
	s_mov_b32 m0, s52
	v_lshl_add_u64 v[232:233], v[232:233], 0, s[36:37]
	ds_read_b128 v[196:199], v157
	ds_read_b128 v[200:203], v157 offset:1024
	ds_read_b128 v[204:207], v157 offset:2048
	ds_read_b128 v[208:211], v157 offset:3072
	ds_read_b128 v[212:215], v157 offset:4096
	ds_read_b128 v[216:219], v157 offset:5120
	ds_read_b128 v[220:223], v157 offset:6144
	ds_read_b128 v[224:227], v157 offset:7168
	global_load_lds_dwordx4 v[232:233], off
	v_lshl_add_u64 v[232:233], v[150:151], 0, s[8:9]
	v_lshl_add_u64 v[232:233], v[232:233], 0, s[36:37]
	s_mov_b32 m0, s53
	s_nop 0
	global_load_lds_dwordx4 v[232:233], off
	s_waitcnt vmcnt(8)
	s_waitcnt lgkmcnt(0)
	s_barrier
	s_setprio 1
	v_mfma_f32_16x16x32_bf16 v[124:127], v[164:167], v[196:199], v[124:127]
	v_mfma_f32_16x16x32_bf16 v[120:123], v[172:175], v[196:199], v[120:123]
	v_mfma_f32_16x16x32_bf16 v[108:111], v[164:167], v[204:207], v[108:111]
	v_mfma_f32_16x16x32_bf16 v[104:107], v[172:175], v[204:207], v[104:107]
	v_mfma_f32_16x16x32_bf16 v[92:95], v[164:167], v[212:215], v[92:95]
	v_mfma_f32_16x16x32_bf16 v[88:91], v[172:175], v[212:215], v[88:91]
	v_mfma_f32_16x16x32_bf16 v[76:79], v[164:167], v[220:223], v[76:79]
	v_mfma_f32_16x16x32_bf16 v[72:75], v[172:175], v[220:223], v[72:75]
	v_mfma_f32_16x16x32_bf16 v[124:127], v[168:171], v[200:203], v[124:127]
	v_mfma_f32_16x16x32_bf16 v[120:123], v[176:179], v[200:203], v[120:123]
	v_mfma_f32_16x16x32_bf16 v[108:111], v[168:171], v[208:211], v[108:111]
	v_mfma_f32_16x16x32_bf16 v[104:107], v[176:179], v[208:211], v[104:107]
	v_mfma_f32_16x16x32_bf16 v[92:95], v[168:171], v[216:219], v[92:95]
	v_mfma_f32_16x16x32_bf16 v[88:91], v[176:179], v[216:219], v[88:91]
	v_mfma_f32_16x16x32_bf16 v[76:79], v[168:171], v[224:227], v[76:79]
	v_mfma_f32_16x16x32_bf16 v[72:75], v[176:179], v[224:227], v[72:75]
	s_setprio 0
	s_setprio 1
	v_mfma_f32_16x16x32_bf16 v[116:119], v[180:183], v[196:199], v[116:119]
	v_mfma_f32_16x16x32_bf16 v[112:115], v[188:191], v[196:199], v[112:115]
	v_mfma_f32_16x16x32_bf16 v[100:103], v[180:183], v[204:207], v[100:103]
	v_mfma_f32_16x16x32_bf16 v[96:99], v[188:191], v[204:207], v[96:99]
	v_mfma_f32_16x16x32_bf16 v[84:87], v[180:183], v[212:215], v[84:87]
	v_mfma_f32_16x16x32_bf16 v[80:83], v[188:191], v[212:215], v[80:83]
	v_mfma_f32_16x16x32_bf16 v[68:71], v[180:183], v[220:223], v[68:71]
	v_mfma_f32_16x16x32_bf16 v[64:67], v[188:191], v[220:223], v[64:67]
	v_mfma_f32_16x16x32_bf16 v[116:119], v[184:187], v[200:203], v[116:119]
	v_mfma_f32_16x16x32_bf16 v[112:115], v[192:195], v[200:203], v[112:115]
	v_mfma_f32_16x16x32_bf16 v[100:103], v[184:187], v[208:211], v[100:103]
	v_mfma_f32_16x16x32_bf16 v[96:99], v[192:195], v[208:211], v[96:99]
	v_mfma_f32_16x16x32_bf16 v[84:87], v[184:187], v[216:219], v[84:87]
	v_mfma_f32_16x16x32_bf16 v[80:83], v[192:195], v[216:219], v[80:83]
	v_mfma_f32_16x16x32_bf16 v[68:71], v[184:187], v[224:227], v[68:71]
	v_mfma_f32_16x16x32_bf16 v[64:67], v[192:195], v[224:227], v[64:67]
	s_setprio 0
	s_barrier
	s_mov_b32 m0, s55
	v_lshl_add_u64 v[232:233], v[230:231], 0, v[128:129]
	ds_read_b128 v[196:199], v157 offset:16384
	ds_read_b128 v[200:203], v157 offset:17408
	ds_read_b128 v[204:207], v157 offset:18432
	ds_read_b128 v[208:211], v157 offset:19456
	ds_read_b128 v[212:215], v157 offset:20480
	ds_read_b128 v[216:219], v157 offset:21504
	ds_read_b128 v[220:223], v157 offset:22528
	ds_read_b128 v[224:227], v157 offset:23552
	global_load_lds_dwordx4 v[232:233], off
	v_lshl_add_u64 v[234:235], v[230:231], 0, v[130:131]
	s_mov_b32 m0, s57
	v_lshl_add_u64 v[236:237], v[230:231], 0, s[24:25]
	global_load_lds_dwordx4 v[234:235], off
	v_lshl_add_u64 v[238:239], v[236:237], 0, v[128:129]
	s_mov_b32 m0, s59
	v_lshl_add_u64 v[236:237], v[236:237], 0, v[130:131]
	global_load_lds_dwordx4 v[238:239], off
	s_mov_b32 m0, s60
	v_mov_b32_e32 v229, v133
	global_load_lds_dwordx4 v[236:237], off
	s_mov_b32 m0, s1
	v_lshl_add_u64 v[236:237], s[40:41], 0, v[132:133]
	global_load_lds_dwordx4 v132, s[40:41]
	s_mov_b32 m0, s22
	s_nop 0
	global_load_lds_dwordx4 v228, s[40:41]
	s_waitcnt vmcnt(8)
	s_waitcnt lgkmcnt(0)
	v_lshl_add_u64 v[228:229], s[40:41], 0, v[228:229]
	s_barrier
	s_setprio 1
	v_mfma_f32_16x16x32_bf16 v[60:63], v[164:167], v[196:199], v[60:63]
	v_mfma_f32_16x16x32_bf16 v[56:59], v[172:175], v[196:199], v[56:59]
	v_mfma_f32_16x16x32_bf16 v[44:47], v[164:167], v[204:207], v[44:47]
	v_mfma_f32_16x16x32_bf16 v[36:39], v[172:175], v[204:207], v[36:39]
	v_mfma_f32_16x16x32_bf16 v[20:23], v[164:167], v[212:215], v[20:23]
	v_mfma_f32_16x16x32_bf16 v[8:11], v[172:175], v[212:215], v[8:11]
	v_mfma_f32_16x16x32_bf16 v[4:7], v[164:167], v[220:223], v[4:7]
	v_mfma_f32_16x16x32_bf16 v[0:3], v[172:175], v[220:223], v[0:3]
	v_mfma_f32_16x16x32_bf16 v[60:63], v[168:171], v[200:203], v[60:63]
	v_mfma_f32_16x16x32_bf16 v[56:59], v[176:179], v[200:203], v[56:59]
	v_mfma_f32_16x16x32_bf16 v[44:47], v[168:171], v[208:211], v[44:47]
	v_mfma_f32_16x16x32_bf16 v[36:39], v[176:179], v[208:211], v[36:39]
	v_mfma_f32_16x16x32_bf16 v[20:23], v[168:171], v[216:219], v[20:23]
	v_mfma_f32_16x16x32_bf16 v[8:11], v[176:179], v[216:219], v[8:11]
	v_mfma_f32_16x16x32_bf16 v[4:7], v[168:171], v[224:227], v[4:7]
	v_mfma_f32_16x16x32_bf16 v[0:3], v[176:179], v[224:227], v[0:3]
	s_setprio 0
	s_setprio 1
	v_mfma_f32_16x16x32_bf16 v[52:55], v[180:183], v[196:199], v[52:55]
	v_mfma_f32_16x16x32_bf16 v[48:51], v[188:191], v[196:199], v[48:51]
	v_mfma_f32_16x16x32_bf16 v[28:31], v[180:183], v[204:207], v[28:31]
	v_mfma_f32_16x16x32_bf16 v[24:27], v[188:191], v[204:207], v[24:27]
	v_mfma_f32_16x16x32_bf16 v[40:43], v[180:183], v[212:215], v[40:43]
	v_mfma_f32_16x16x32_bf16 v[32:35], v[188:191], v[212:215], v[32:35]
	v_mfma_f32_16x16x32_bf16 v[16:19], v[180:183], v[220:223], v[16:19]
	v_mfma_f32_16x16x32_bf16 v[12:15], v[188:191], v[220:223], v[12:15]
	v_mfma_f32_16x16x32_bf16 v[52:55], v[184:187], v[200:203], v[52:55]
	v_mfma_f32_16x16x32_bf16 v[48:51], v[192:195], v[200:203], v[48:51]
	v_mfma_f32_16x16x32_bf16 v[28:31], v[184:187], v[208:211], v[28:31]
	v_mfma_f32_16x16x32_bf16 v[24:27], v[192:195], v[208:211], v[24:27]
	v_mfma_f32_16x16x32_bf16 v[40:43], v[184:187], v[216:219], v[40:43]
	v_mfma_f32_16x16x32_bf16 v[32:35], v[192:195], v[216:219], v[32:35]
	v_mfma_f32_16x16x32_bf16 v[16:19], v[184:187], v[224:227], v[16:19]
	v_mfma_f32_16x16x32_bf16 v[12:15], v[192:195], v[224:227], v[12:15]
	s_setprio 0
	s_barrier
	v_add_u32_e32 v132, s61, v143
	s_add_i32 s51, 0, 0x1c000
	ds_read_b128 v[164:167], v132
	ds_read_b128 v[168:171], v132 offset:1024
	ds_read_b128 v[172:175], v132 offset:2048
	ds_read_b128 v[176:179], v132 offset:3072
	v_add_u32_e32 v132, s51, v143
	ds_read_b128 v[180:183], v132
	ds_read_b128 v[184:187], v132 offset:1024
	ds_read_b128 v[188:191], v132 offset:2048
	ds_read_b128 v[192:195], v132 offset:3072
	s_mov_b32 m0, s42
	ds_read_b128 v[196:199], v157 offset:32768
	ds_read_b128 v[200:203], v157 offset:33792
	ds_read_b128 v[204:207], v157 offset:34816
	ds_read_b128 v[208:211], v157 offset:35840
	ds_read_b128 v[212:215], v157 offset:36864
	ds_read_b128 v[216:219], v157 offset:37888
	ds_read_b128 v[220:223], v157 offset:38912
	ds_read_b128 v[224:227], v157 offset:39936
	global_load_lds_dwordx4 v139, s[40:41]
	s_mov_b32 m0, s43
	s_nop 0
	global_load_lds_dwordx4 v141, s[40:41]
	s_waitcnt vmcnt(8)
	s_waitcnt lgkmcnt(0)
	s_barrier
	s_setprio 1
	v_mfma_f32_16x16x32_bf16 v[124:127], v[164:167], v[196:199], v[124:127]
	v_mfma_f32_16x16x32_bf16 v[120:123], v[172:175], v[196:199], v[120:123]
	v_mfma_f32_16x16x32_bf16 v[108:111], v[164:167], v[204:207], v[108:111]
	v_mfma_f32_16x16x32_bf16 v[104:107], v[172:175], v[204:207], v[104:107]
	v_mfma_f32_16x16x32_bf16 v[92:95], v[164:167], v[212:215], v[92:95]
	v_mfma_f32_16x16x32_bf16 v[88:91], v[172:175], v[212:215], v[88:91]
	v_mfma_f32_16x16x32_bf16 v[76:79], v[164:167], v[220:223], v[76:79]
	v_mfma_f32_16x16x32_bf16 v[72:75], v[172:175], v[220:223], v[72:75]
	v_mfma_f32_16x16x32_bf16 v[124:127], v[168:171], v[200:203], v[124:127]
	v_mfma_f32_16x16x32_bf16 v[120:123], v[176:179], v[200:203], v[120:123]
	v_mfma_f32_16x16x32_bf16 v[108:111], v[168:171], v[208:211], v[108:111]
	v_mfma_f32_16x16x32_bf16 v[104:107], v[176:179], v[208:211], v[104:107]
	v_mfma_f32_16x16x32_bf16 v[92:95], v[168:171], v[216:219], v[92:95]
	v_mfma_f32_16x16x32_bf16 v[88:91], v[176:179], v[216:219], v[88:91]
	v_mfma_f32_16x16x32_bf16 v[76:79], v[168:171], v[224:227], v[76:79]
	v_mfma_f32_16x16x32_bf16 v[72:75], v[176:179], v[224:227], v[72:75]
	s_setprio 0
	s_setprio 1
	v_mfma_f32_16x16x32_bf16 v[116:119], v[180:183], v[196:199], v[116:119]
	v_mfma_f32_16x16x32_bf16 v[112:115], v[188:191], v[196:199], v[112:115]
	v_mfma_f32_16x16x32_bf16 v[100:103], v[180:183], v[204:207], v[100:103]
	v_mfma_f32_16x16x32_bf16 v[96:99], v[188:191], v[204:207], v[96:99]
	v_mfma_f32_16x16x32_bf16 v[84:87], v[180:183], v[212:215], v[84:87]
	v_mfma_f32_16x16x32_bf16 v[80:83], v[188:191], v[212:215], v[80:83]
	v_mfma_f32_16x16x32_bf16 v[68:71], v[180:183], v[220:223], v[68:71]
	v_mfma_f32_16x16x32_bf16 v[64:67], v[188:191], v[220:223], v[64:67]
	v_mfma_f32_16x16x32_bf16 v[116:119], v[184:187], v[200:203], v[116:119]
	v_mfma_f32_16x16x32_bf16 v[112:115], v[192:195], v[200:203], v[112:115]
	v_mfma_f32_16x16x32_bf16 v[100:103], v[184:187], v[208:211], v[100:103]
	v_mfma_f32_16x16x32_bf16 v[96:99], v[192:195], v[208:211], v[96:99]
	v_mfma_f32_16x16x32_bf16 v[84:87], v[184:187], v[216:219], v[84:87]
	v_mfma_f32_16x16x32_bf16 v[80:83], v[192:195], v[216:219], v[80:83]
	v_mfma_f32_16x16x32_bf16 v[68:71], v[184:187], v[224:227], v[68:71]
	v_mfma_f32_16x16x32_bf16 v[64:67], v[192:195], v[224:227], v[64:67]
	s_setprio 0
	s_barrier
	s_add_i32 s40, s61, s0
	v_lshl_add_u64 v[232:233], v[232:233], 0, s[28:29]
	s_mov_b32 m0, s40
	ds_read_b128 v[196:199], v157 offset:49152
	ds_read_b128 v[200:203], v157 offset:50176
	ds_read_b128 v[204:207], v157 offset:51200
	ds_read_b128 v[208:211], v157 offset:52224
	ds_read_b128 v[212:215], v157 offset:53248
	ds_read_b128 v[216:219], v157 offset:54272
	ds_read_b128 v[220:223], v157 offset:55296
	ds_read_b128 v[224:227], v157 offset:56320
	global_load_lds_dwordx4 v[232:233], off
	v_lshl_add_u64 v[232:233], v[234:235], 0, s[28:29]
	s_add_i32 m0, s40, 0x2000
	v_lshl_add_u64 v[230:231], v[230:231], 0, s[30:31]
	s_add_i32 s40, s51, s0
	global_load_lds_dwordx4 v[232:233], off
	v_lshl_add_u64 v[232:233], v[230:231], 0, v[128:129]
	s_mov_b32 m0, s40
	v_lshl_add_u64 v[230:231], v[230:231], 0, v[130:131]
	global_load_lds_dwordx4 v[232:233], off
	s_add_i32 m0, s40, 0x2000
	v_lshl_add_u64 v[228:229], v[228:229], 0, s[28:29]
	global_load_lds_dwordx4 v[230:231], off
	v_lshl_add_u64 v[230:231], v[236:237], 0, s[28:29]
	s_mov_b32 m0, s46
	s_nop 0
	global_load_lds_dwordx4 v[230:231], off
	s_mov_b32 m0, s47
	s_nop 0
	global_load_lds_dwordx4 v[228:229], off
	s_waitcnt vmcnt(8)
	s_waitcnt lgkmcnt(0)
	s_barrier
	s_setprio 1
	v_mfma_f32_16x16x32_bf16 v[60:63], v[164:167], v[196:199], v[60:63]
	v_mfma_f32_16x16x32_bf16 v[56:59], v[172:175], v[196:199], v[56:59]
	v_mfma_f32_16x16x32_bf16 v[44:47], v[164:167], v[204:207], v[44:47]
	v_mfma_f32_16x16x32_bf16 v[36:39], v[172:175], v[204:207], v[36:39]
	v_mfma_f32_16x16x32_bf16 v[20:23], v[164:167], v[212:215], v[20:23]
	v_mfma_f32_16x16x32_bf16 v[8:11], v[172:175], v[212:215], v[8:11]
	v_mfma_f32_16x16x32_bf16 v[4:7], v[164:167], v[220:223], v[4:7]
	v_mfma_f32_16x16x32_bf16 v[0:3], v[172:175], v[220:223], v[0:3]
	v_mfma_f32_16x16x32_bf16 v[60:63], v[168:171], v[200:203], v[60:63]
	v_mfma_f32_16x16x32_bf16 v[56:59], v[176:179], v[200:203], v[56:59]
	v_mfma_f32_16x16x32_bf16 v[44:47], v[168:171], v[208:211], v[44:47]
	v_mfma_f32_16x16x32_bf16 v[36:39], v[176:179], v[208:211], v[36:39]
	v_mfma_f32_16x16x32_bf16 v[20:23], v[168:171], v[216:219], v[20:23]
	v_mfma_f32_16x16x32_bf16 v[8:11], v[176:179], v[216:219], v[8:11]
	v_mfma_f32_16x16x32_bf16 v[4:7], v[168:171], v[224:227], v[4:7]
	v_mfma_f32_16x16x32_bf16 v[0:3], v[176:179], v[224:227], v[0:3]
	s_setprio 0
	s_setprio 1
	v_mfma_f32_16x16x32_bf16 v[52:55], v[180:183], v[196:199], v[52:55]
	v_mfma_f32_16x16x32_bf16 v[48:51], v[188:191], v[196:199], v[48:51]
	v_mfma_f32_16x16x32_bf16 v[28:31], v[180:183], v[204:207], v[28:31]
	v_mfma_f32_16x16x32_bf16 v[24:27], v[188:191], v[204:207], v[24:27]
	v_mfma_f32_16x16x32_bf16 v[40:43], v[180:183], v[212:215], v[40:43]
	v_mfma_f32_16x16x32_bf16 v[32:35], v[188:191], v[212:215], v[32:35]
	v_mfma_f32_16x16x32_bf16 v[16:19], v[180:183], v[220:223], v[16:19]
	v_mfma_f32_16x16x32_bf16 v[12:15], v[188:191], v[220:223], v[12:15]
	v_mfma_f32_16x16x32_bf16 v[52:55], v[184:187], v[200:203], v[52:55]
	v_mfma_f32_16x16x32_bf16 v[48:51], v[192:195], v[200:203], v[48:51]
	v_mfma_f32_16x16x32_bf16 v[28:31], v[184:187], v[208:211], v[28:31]
	v_mfma_f32_16x16x32_bf16 v[24:27], v[192:195], v[208:211], v[24:27]
	v_mfma_f32_16x16x32_bf16 v[40:43], v[184:187], v[216:219], v[40:43]
	v_mfma_f32_16x16x32_bf16 v[32:35], v[192:195], v[216:219], v[32:35]
	v_mfma_f32_16x16x32_bf16 v[16:19], v[184:187], v[224:227], v[16:19]
	v_mfma_f32_16x16x32_bf16 v[12:15], v[192:195], v[224:227], v[12:15]
	s_setprio 0
	s_barrier
	s_add_i32 s39, s39, 2
	s_add_u32 s8, s8, 0x100
	s_addc_u32 s9, s9, 0
	s_cmp_gt_u32 s39, 29
	s_cbranch_scc0 .LBB0_2750
	s_and_b64 vcc, exec, s[34:35]
	s_cbranch_vccz .LBB0_2753
	s_barrier
